# baseline (speedup 1.0000x reference)
_Z11prep_kernelPKfS0_S0_S0_S0_PKiPDF16_S3_S3_PyPi:
	s_cmpk_gt_i32 s2, 0x7ff
	s_mov_b64 s[4:5], -1
	s_cbranch_scc0 .LBB0_22
	s_cmpk_gt_u32 s2, 0xbff
	v_lshrrev_b32_e32 v1, 6, v0
	v_and_b32_e32 v2, 63, v0
	s_cbranch_scc0 .LBB0_11
	s_cmpk_lg_u32 s2, 0xc00
	s_cbranch_scc1 .Lprep_mdone
	s_load_dwordx2 s[4:5], s[0:1], 0x28
	s_load_dwordx2 s[6:7], s[0:1], 0x50
	v_cmp_eq_u32_e32 vcc, 0, v0
	s_and_saveexec_b64 s[8:9], vcc
	s_cbranch_execz .Lprep_mdone
	s_waitcnt lgkmcnt(0)
	v_mov_b32_e32 v2, s4
	v_mov_b32_e32 v3, s5
	v_mov_b32_e32 v4, 0x2000
	global_store_dwordx2 v4, v[2:3], s[6:7]
.Lprep_mdone:
	s_endpgm
.LBB0_11:
	s_and_b64 vcc, exec, s[4:5]
	s_cbranch_vccz .LBB0_20
	s_load_dwordx8 s[4:11], s[0:1], 0x8
	s_add_i32 s14, s2, 0xfffff800
	s_lshr_b32 s3, s14, 8
	s_bfe_u32 s13, s2, 0x40004
	s_and_b32 s12, s2, 15
	s_cmpk_lt_u32 s14, 0x100
	s_cselect_b64 vcc, -1, 0
	s_cmp_eq_u32 s3, 2
	s_waitcnt lgkmcnt(0)
	s_cselect_b32 s9, s9, s11
	s_cselect_b32 s8, s8, s10
	s_cmp_eq_u32 s3, 1
	s_cselect_b32 s8, s6, s8
	s_cselect_b32 s9, s7, s9
	s_and_b64 s[6:7], vcc, exec
	s_cselect_b32 s5, s5, s9
	s_cselect_b32 s4, s4, s8
	s_lshl_b32 s6, s12, 8
	s_add_u32 s4, s4, s6
	v_mov_b32_e32 v3, 0x3e38aa3b
	s_addc_u32 s5, s5, 0
	v_lshlrev_b32_e32 v8, 2, v2
	v_mov_b32_e32 v9, 0
	v_cndmask_b32_e32 v6, 1.0, v3, vcc
	v_lshl_add_u64 v[2:3], s[4:5], 0, v[8:9]
	s_lshl_b32 s4, s13, 18
	v_lshl_or_b32 v4, v1, 12, s4
	v_mov_b32_e32 v5, v9
	v_lshl_add_u64 v[10:11], v[2:3], 0, v[4:5]
	v_or_b32_e32 v5, 0x200, v0
	v_lshrrev_b32_e32 v13, 6, v5
	v_or_b32_e32 v5, 0x300, v0
	v_lshrrev_b32_e32 v28, 6, v5
	v_or_b32_e32 v5, 0x500, v0
	v_lshrrev_b32_e32 v29, 6, v5
	v_or_b32_e32 v5, 0x600, v0
	v_or_b32_e32 v12, 0x100, v0
	v_lshrrev_b32_e32 v30, 6, v5
	v_or_b32_e32 v5, 0x700, v0
	v_lshrrev_b32_e32 v7, 6, v12
	v_lshl_or_b32 v22, v29, 12, s4
	v_mov_b32_e32 v23, v9
	v_lshrrev_b32_e32 v31, 6, v5
	v_lshl_or_b32 v14, v7, 12, s4
	v_mov_b32_e32 v15, v9
	v_lshl_or_b32 v16, v13, 12, s4
	v_mov_b32_e32 v17, v9
	v_lshl_or_b32 v18, v28, 12, s4
	v_mov_b32_e32 v19, v9
	v_or_b32_e32 v20, 0x10000, v4
	v_mov_b32_e32 v21, v9
	v_lshl_add_u64 v[22:23], v[2:3], 0, v[22:23]
	v_lshl_or_b32 v24, v30, 12, s4
	v_mov_b32_e32 v25, v9
	v_lshl_or_b32 v26, v31, 12, s4
	v_mov_b32_e32 v27, v9
	v_or_b32_e32 v5, 0x900, v0
	v_lshl_add_u64 v[14:15], v[2:3], 0, v[14:15]
	v_lshl_add_u64 v[16:17], v[2:3], 0, v[16:17]
	v_lshl_add_u64 v[18:19], v[2:3], 0, v[18:19]
	v_lshl_add_u64 v[20:21], v[2:3], 0, v[20:21]
	v_lshl_add_u64 v[24:25], v[2:3], 0, v[24:25]
	v_lshl_add_u64 v[26:27], v[2:3], 0, v[26:27]
	global_load_dword v32, v[10:11], off nt
	global_load_dword v33, v[14:15], off nt
	global_load_dword v34, v[16:17], off nt
	global_load_dword v35, v[18:19], off nt
	global_load_dword v36, v[20:21], off nt
	global_load_dword v37, v[22:23], off nt
	global_load_dword v38, v[24:25], off nt
	global_load_dword v39, v[26:27], off nt
	v_or_b32_e32 v10, 0x20000, v4
	v_mov_b32_e32 v11, v9
	v_lshrrev_b32_e32 v23, 6, v5
	v_or_b32_e32 v5, 0xa00, v0
	v_lshl_add_u64 v[10:11], v[2:3], 0, v[10:11]
	v_lshrrev_b32_e32 v24, 6, v5
	v_or_b32_e32 v5, 0xb00, v0
	v_or_b32_e32 v18, 0xd00, v0
	v_or_b32_e32 v20, 0xe00, v0
	global_load_dword v22, v[10:11], off nt
	v_lshl_or_b32 v10, v23, 12, s4
	v_mov_b32_e32 v11, v9
	v_lshrrev_b32_e32 v25, 6, v5
	v_or_b32_e32 v4, 0x30000, v4
	v_mov_b32_e32 v5, v9
	v_lshrrev_b32_e32 v26, 6, v18
	v_lshrrev_b32_e32 v27, 6, v20
	v_lshl_add_u64 v[10:11], v[2:3], 0, v[10:11]
	v_lshl_or_b32 v14, v24, 12, s4
	v_mov_b32_e32 v15, v9
	v_lshl_or_b32 v16, v25, 12, s4
	v_mov_b32_e32 v17, v9
	v_lshl_add_u64 v[4:5], v[2:3], 0, v[4:5]
	v_lshl_or_b32 v18, v26, 12, s4
	v_mov_b32_e32 v19, v9
	v_lshl_or_b32 v20, v27, 12, s4
	v_mov_b32_e32 v21, v9
	v_lshl_add_u64 v[14:15], v[2:3], 0, v[14:15]
	v_lshl_add_u64 v[16:17], v[2:3], 0, v[16:17]
	v_lshl_add_u64 v[18:19], v[2:3], 0, v[18:19]
	v_lshl_add_u64 v[20:21], v[2:3], 0, v[20:21]
	global_load_dword v40, v[10:11], off nt
	global_load_dword v41, v[14:15], off nt
	global_load_dword v42, v[16:17], off nt
	global_load_dword v43, v[4:5], off nt
	global_load_dword v44, v[18:19], off nt
	global_load_dword v45, v[20:21], off nt
	v_or_b32_e32 v4, 0xf00, v0
	v_lshrrev_b32_e32 v10, 6, v4
	v_lshl_or_b32 v4, v10, 12, s4
	v_mov_b32_e32 v5, v9
	v_lshl_add_u64 v[2:3], v[2:3], 0, v[4:5]
	global_load_dword v2, v[2:3], off nt
	s_movk_i32 s8, 0x104
	v_mad_u32_u24 v1, v1, s8, v8
	v_mad_u32_u24 v3, v7, s8, v8
	s_cmpk_gt_u32 s14, 0x2ff
	v_lshrrev_b32_e32 v7, 3, v0
	s_movk_i32 s11, 0x820
	s_load_dwordx4 s[4:7], s[0:1], 0x38
	v_bfe_u32 v14, v0, 3, 2
	s_waitcnt vmcnt(15)
	ds_write_b32 v1, v32
	s_waitcnt vmcnt(14)
	ds_write_b32 v3, v33
	v_mad_u32_u24 v3, v13, s8, v8
	s_waitcnt vmcnt(13)
	ds_write_b32 v3, v34
	v_mad_u32_u24 v3, v28, s8, v8
	s_waitcnt vmcnt(12)
	ds_write_b32 v3, v35
	s_waitcnt vmcnt(11)
	ds_write_b32 v1, v36 offset:4160
	v_mad_u32_u24 v3, v29, s8, v8
	s_waitcnt vmcnt(10)
	ds_write_b32 v3, v37
	v_mad_u32_u24 v3, v30, s8, v8
	s_waitcnt vmcnt(9)
	ds_write_b32 v3, v38
	v_mad_u32_u24 v3, v31, s8, v8
	s_waitcnt vmcnt(8)
	ds_write_b32 v3, v39
	s_waitcnt vmcnt(7)
	ds_write_b32 v1, v22 offset:8320
	v_mad_u32_u24 v3, v23, s8, v8
	s_waitcnt vmcnt(6)
	ds_write_b32 v3, v40
	v_mad_u32_u24 v3, v24, s8, v8
	s_waitcnt vmcnt(5)
	ds_write_b32 v3, v41
	v_mad_u32_u24 v3, v25, s8, v8
	s_waitcnt vmcnt(4)
	ds_write_b32 v3, v42
	s_waitcnt vmcnt(3)
	ds_write_b32 v1, v43 offset:12480
	v_mad_u32_u24 v1, v26, s8, v8
	s_waitcnt vmcnt(2)
	ds_write_b32 v1, v44
	v_mad_u32_u24 v1, v27, s8, v8
	s_waitcnt vmcnt(1)
	ds_write_b32 v1, v45
	v_mad_u32_u24 v1, v10, s8, v8
	v_lshrrev_b32_e32 v3, 4, v0
	s_waitcnt vmcnt(0)
	ds_write_b32 v1, v2
	v_lshrrev_b32_e32 v2, 1, v0
	s_cselect_b64 s[8:9], -1, 0
	s_lshl_b32 s10, s12, 16
	v_and_b32_e32 v2, 16, v2
	v_and_b32_e32 v3, 12, v3
	s_mulk_i32 s12, 0xc0
	v_or3_b32 v2, v2, v3, s12
	v_and_b32_e32 v1, 7, v0
	v_lshl_add_u32 v13, s3, 5, v2
	v_lshlrev_b32_e32 v2, 2, v7
	v_mad_u32_u24 v4, v1, s11, v2
	s_waitcnt lgkmcnt(0)
	s_barrier
	ds_read2_b32 v[2:3], v4 offset1:65
	ds_read2_b32 v[16:17], v4 offset0:130 offset1:195
	v_add_u32_e32 v15, 0x400, v4
	ds_read2_b32 v[18:19], v15 offset0:4 offset1:69
	s_lshl_b32 s13, s13, 7
	s_waitcnt lgkmcnt(2)
	v_fma_mixlo_f16 v5, v6, v2, 0
	v_mov_b32_e32 v2, v3
	s_waitcnt lgkmcnt(1)
	v_mov_b32_e32 v3, v16
	v_mov_b32_e32 v4, v17
	ds_read2_b32 v[16:17], v15 offset0:134 offset1:199
	v_pk_mul_f32 v[2:3], v[6:7], v[2:3] op_sel_hi:[0,1]
	v_cvt_pk_f16_f32 v3, v2, v3
	v_pack_b32_f16 v2, v5, v3
	s_waitcnt lgkmcnt(1)
	v_mov_b32_e32 v5, v18
	v_pk_mul_f32 v[4:5], v[6:7], v[4:5] op_sel_hi:[0,1]
	v_cvt_pk_f16_f32 v15, v4, v5
	v_mov_b32_e32 v4, v19
	s_waitcnt lgkmcnt(0)
	v_mov_b32_e32 v5, v16
	s_add_u32 s6, s6, s13
	v_pk_mul_f32 v[4:5], v[6:7], v[4:5] op_sel_hi:[0,1]
	s_addc_u32 s7, s7, 0
	v_cvt_pk_f16_f32 v5, v4, v5
	v_lshlrev_b32_e32 v8, 4, v1
	s_add_u32 s4, s4, s13
	v_alignbit_b32 v4, v5, v15, 16
	v_lshrrev_b32_e32 v5, 16, v5
	v_lshl_add_u64 v[10:11], s[6:7], 0, v[8:9]
	s_addc_u32 s5, s5, 0
	v_alignbit_b32 v3, v15, v3, 16
	v_fma_mixhi_f16 v5, v6, v17, 0
	s_mov_b64 s[6:7], -1
	s_and_b64 vcc, exec, s[8:9]
	s_cbranch_vccz .LBB0_14
	v_lshlrev_b32_e32 v7, 10, v7
	v_add_lshl_u32 v16, v7, s10, 1
	v_mov_b32_e32 v17, v9
	v_lshl_add_u64 v[16:17], v[10:11], 0, v[16:17]
	global_store_dwordx4 v[16:17], v[2:5], off sc1
	s_mov_b64 s[6:7], 0

.LBB1_6:
	v_and_b32_e32 v1, 31, v0
	v_lshl_or_b32 v2, s10, 5, v1
	v_ashrrev_i32_e32 v3, 31, v2
	s_waitcnt lgkmcnt(0)
	v_lshl_add_u64 v[2:3], v[2:3], 2, s[4:5]
	global_load_dword v104, v[2:3], off
	s_mov_b32 s11, 0
	v_lshrrev_b32_e32 v2, 2, v0
	v_and_b32_e32 v1, 15, v0
	s_lshl_b32 s5, s10, 6
	v_and_b32_e32 v2, 48, v2
	s_and_b32 s3, s2, 31
	v_or3_b32 v86, s5, v2, v1
	s_lshl_b32 s10, s3, 11
	v_ashrrev_i32_e32 v87, 31, v86
	v_lshl_add_u64 v[2:3], v[86:87], 0, s[10:11]
	v_lshlrev_b64 v[2:3], 7, v[2:3]
	v_lshl_add_u64 v[2:3], s[12:13], 0, v[2:3]
	v_mov_b32_e32 v5, 0
	v_and_b32_e32 v4, 48, v0
	v_lshl_add_u64 v[10:11], v[2:3], 0, v[4:5]
	global_load_dwordx4 v[2:5], v[10:11], off
	global_load_dwordx4 v[6:9], v[10:11], off offset:64
	v_bfe_u32 v10, v0, 4, 2
	v_and_b32_e32 v11, 63, v0
	v_lshlrev_b32_e32 v88, 3, v10
	s_lshl_b32 s1, s10, 7
	v_lshrrev_b32_e32 v13, 3, v0
	s_add_u32 s12, s14, s1
	v_mov_b32_e32 v12, 0
	v_lshlrev_b32_e32 v32, 7, v13
	s_addc_u32 s13, s15, 0
	v_mov_b32_e32 v33, v12
	v_lshl_add_u64 v[14:15], s[12:13], 0, v[32:33]
	s_add_u32 s12, s16, s1
	v_lshlrev_b32_e32 v90, 4, v0
	s_addc_u32 s13, s17, 0
	v_mov_b32_e32 v91, v12
	v_lshl_add_u64 v[94:95], s[12:13], 0, v[90:91]
	v_and_b32_e32 v16, 0x70, v90
	v_mov_b32_e32 v17, v12
	v_lshl_add_u64 v[92:93], v[14:15], 0, v[16:17]
	v_lshl_add_u64 v[96:97], v[86:87], 3, s[18:19]
	s_mov_b32 s0, 0
	s_lshl_b32 s12, s0, 6
	s_ashr_i32 s1, s0, 31
	s_lshl_b64 s[14:15], s[0:1], 13
	s_ashr_i32 s13, s12, 31
	v_lshl_add_u64 v[26:27], v[94:95], 0, s[14:15]
	s_lshl_b64 s[14:15], s[12:13], 7
	s_or_b32 s12, s12, 32
	s_movk_i32 s5, 0x1000
	global_load_dwordx4 v[14:17], v[26:27], off
	s_ashr_i32 s13, s12, 31
	v_add_co_u32_e32 v26, vcc, s5, v26
	v_lshl_add_u64 v[28:29], v[92:93], 0, s[14:15]
	s_lshl_b64 s[12:13], s[12:13], 7
	v_addc_co_u32_e32 v27, vcc, 0, v27, vcc
	v_lshl_add_u64 v[30:31], v[92:93], 0, s[12:13]
	global_load_dwordx4 v[22:25], v[28:29], off
	global_load_dwordx4 v[18:21], v[30:31], off
	global_load_dwordx4 v[26:29], v[26:27], off
	s_lshl_b64 s[12:13], s[0:1], 14
	v_lshl_add_u64 v[30:31], v[96:97], 0, s[12:13]
	global_load_dwordx2 v[102:103], v[30:31], off
	s_waitcnt vmcnt(7)
	s_mov_b32 s22, 0x2020202
	s_mov_b32 s23, 0x4040404
	v_and_b32_e32 v105, 0x1010101, v104
	v_and_b32_e32 v106, s22, v104
	v_and_b32_e32 v107, s23, v104
	v_cmp_ne_u32_e64 s[8:9], 0, v105
	v_cmp_eq_u32_e64 s[6:7], s22, v106
	v_cmp_eq_u32_e64 s[4:5], s23, v107
	s_nop 1
	s_andn2_b64 s[4:5], s[4:5], s[6:7]
	s_and_b64 s[4:5], s[4:5], s[8:9]
	s_cmp_eq_u32 s8, 0
	s_cbranch_scc1 .LBB1_48
	s_branch .LBB1_10

_Z9gemm_gldsILi256ELi192ELi4ELi2ELi2ELi4ELi8ELi0ELi4096ELi3072ELi1024EEvPKDF16_S1_PfPKfS4_PKiPDF16_S7_S7_:
	s_mov_b32 s47, s2
	s_ashr_i32 s3, s2, 3
	s_lshr_b32 s9, s3, 30
	s_add_i32 s9, s3, s9
	s_lshl_b32 s8, s2, 1
	s_ashr_i32 s10, s9, 2
	s_and_b32 s9, s9, 0xfffffc
	s_lshl_b32 s2, s2, 3
	s_load_dwordx4 s[4:7], s[0:1], 0x0
	s_and_b32 s8, s8, 12
	s_sub_i32 s3, s3, s9
	s_and_b32 s20, s2, 8
	s_add_i32 s8, s8, s3
	s_add_i32 s20, s20, s10
	s_lshl_b32 s16, s8, 8
	s_mul_i32 s2, s20, 0xc0
	v_lshlrev_b32_e32 v139, 4, v0
	v_and_b32_e32 v1, 32, v0
	s_ashr_i32 s17, s16, 31
	s_ashr_i32 s3, s2, 31
	v_lshrrev_b32_e32 v2, 3, v0
	v_bfe_u32 v46, v0, 2, 4
	v_bitop3_b32 v1, v139, v1, 48 bitop3:0x6c
	s_lshl_b64 s[8:9], s[16:17], 11
	s_lshl_b64 s[10:11], s[2:3], 11
	v_and_or_b32 v2, v2, 48, v46
	v_and_or_b32 v47, v0, 64, v1
	s_waitcnt lgkmcnt(0)
	s_add_u32 s50, s4, 0x3082000
	s_addc_u32 s51, s5, 0
	s_load_dwordx2 s[52:53], s[50:51], 0x0
	s_add_u32 s54, s4, 0x3000000
	s_addc_u32 s55, s5, 0
	s_add_u32 s56, s4, 0x3080000
	s_addc_u32 s57, s5, 0
	s_add_u32 s2, s4, s8
	s_addc_u32 s3, s5, s9
	v_lshl_or_b32 v2, v2, 11, v47
	v_mov_b32_e32 v3, 0
	v_readfirstlane_b32 s4, v139
	v_or_b32_e32 v1, 0x2000, v139
	s_add_u32 s18, s6, s10
	v_lshl_add_u64 v[4:5], s[2:3], 0, v[2:3]
	s_mov_b32 m0, s4
	s_mov_b64 s[4:5], 0x20000
	v_readfirstlane_b32 s6, v1
	v_or_b32_e32 v1, 0x4000, v139
	s_addc_u32 s19, s7, s11
	global_load_lds_dwordx4 v2, s[2:3]
	v_lshl_add_u64 v[8:9], v[4:5], 0, s[4:5]
	s_mov_b32 m0, s6
	s_mov_b64 s[6:7], 0x40000
	v_readfirstlane_b32 s8, v1
	global_load_lds_dwordx4 v[8:9], off
	v_lshl_add_u64 v[8:9], v[4:5], 0, s[6:7]
	s_mov_b32 m0, s8
	s_mov_b64 s[8:9], 0x60000
	v_or_b32_e32 v1, 0x6000, v139
	global_load_lds_dwordx4 v[8:9], off
	v_lshl_add_u64 v[8:9], v[4:5], 0, s[8:9]
	v_readfirstlane_b32 s8, v1
	v_or_b32_e32 v1, 0x8000, v139
	v_lshl_add_u64 v[6:7], s[18:19], 0, v[2:3]
	s_mov_b32 m0, s8
	v_readfirstlane_b32 s8, v1
	v_or_b32_e32 v1, 0xa000, v139
	global_load_lds_dwordx4 v[8:9], off
	s_mov_b32 m0, s8
	v_lshl_add_u64 v[8:9], v[6:7], 0, s[4:5]
	v_readfirstlane_b32 s4, v1
	v_or_b32_e32 v1, 0xc000, v139
	global_load_lds_dwordx4 v2, s[18:19]
	s_mov_b32 m0, s4
	v_readfirstlane_b32 s4, v1
	v_or_b32_e32 v1, 0xe000, v139
	global_load_lds_dwordx4 v[8:9], off
	v_lshl_add_u64 v[8:9], v[6:7], 0, s[6:7]
	s_mov_b32 m0, s4
	s_mov_b64 s[4:5], 0x80
	v_readfirstlane_b32 s6, v1
	v_or_b32_e32 v1, 0x10000, v139
	global_load_lds_dwordx4 v[8:9], off
	v_lshl_add_u64 v[8:9], v[4:5], 0, s[4:5]
	s_mov_b32 m0, s6
	s_mov_b64 s[6:7], 0x20080
	v_readfirstlane_b32 s8, v1
	v_or_b32_e32 v1, 0x12000, v139
	global_load_lds_dwordx4 v[8:9], off
	v_lshl_add_u64 v[8:9], v[4:5], 0, s[6:7]
	s_mov_b32 m0, s8
	v_readfirstlane_b32 s10, v1
	global_load_lds_dwordx4 v[8:9], off
	s_mov_b64 s[8:9], 0x40080
	s_mov_b32 m0, s10
	s_mov_b64 s[10:11], 0x60080
	v_or_b32_e32 v1, 0x14000, v139
	v_lshl_add_u64 v[8:9], v[4:5], 0, s[8:9]
	v_lshl_add_u64 v[4:5], v[4:5], 0, s[10:11]
	v_readfirstlane_b32 s10, v1
	global_load_lds_dwordx4 v[8:9], off
	s_mov_b32 m0, s10
	v_or_b32_e32 v1, 0x16000, v139
	global_load_lds_dwordx4 v[4:5], off
	v_lshl_add_u64 v[4:5], v[6:7], 0, s[4:5]
	v_readfirstlane_b32 s4, v1
	v_or_b32_e32 v1, 0x18000, v139
	s_mov_b32 m0, s4
	v_readfirstlane_b32 s4, v1
	v_or_b32_e32 v1, 0x1a000, v139
	global_load_lds_dwordx4 v[4:5], off
	v_lshl_add_u64 v[4:5], v[6:7], 0, s[6:7]
	s_mov_b32 m0, s4
	v_readfirstlane_b32 s4, v1
	global_load_lds_dwordx4 v[4:5], off
	v_lshl_add_u64 v[4:5], v[6:7], 0, s[8:9]
	s_mov_b32 m0, s4
	v_lshrrev_b32_e32 v2, 7, v0
	global_load_lds_dwordx4 v[4:5], off
	s_load_dwordx4 s[12:15], s[0:1], 0x38
	s_load_dwordx8 s[4:11], s[0:1], 0x18
	v_lshlrev_b32_e32 v4, 6, v0
	v_and_b32_e32 v138, 48, v0
	v_and_b32_e32 v4, 0x3c0, v4
	v_lshlrev_b32_e32 v6, 2, v0
	v_bfe_u32 v144, v0, 6, 1
	v_or_b32_e32 v14, v4, v138
	v_lshlrev_b32_e32 v5, 13, v2
	v_and_b32_e32 v15, 32, v6
	v_and_b32_e32 v1, 15, v0
	v_bitop3_b32 v151, v4, v15, v138 bitop3:0x36
	v_bitop3_b32 v146, v5, v14, v15 bitop3:0xf6
	v_mul_u32_u24_e32 v152, 0x3000, v144
	v_lshl_or_b32 v145, v2, 6, s16
	v_or_b32_e32 v4, v145, v1
	v_ashrrev_i32_e32 v5, 31, v4
	s_waitcnt lgkmcnt(0)
	v_lshl_add_u64 v[4:5], v[4:5], 2, s[8:9]
	global_load_dword v150, v[4:5], off
	global_load_dword v149, v[4:5], off offset:64
	global_load_dword v148, v[4:5], off offset:128
	global_load_dword v147, v[4:5], off offset:192
	v_readfirstlane_b32 s48, v0
	v_and_b32_e32 v248, 63, v0
	v_lshlrev_b32_e32 v248, 2, v248
	s_lshr_b32 s48, s48, 6
	s_and_b32 s49, s48, 1
	s_lshr_b32 s48, s48, 1
	s_lshr_b32 s58, s47, 3
	s_lshl_b32 s58, s58, 6
	s_lshl_b32 s61, s49, 5
	s_add_u32 s58, s58, s61
	s_and_b32 s59, s47, 7
	s_lshl_b32 s59, s59, 2
	s_add_u32 s59, s59, s48
	s_lshl_b32 s60, s47, 2
	s_add_u32 s60, s60, s48
	s_lshl_b32 s60, s60, 2
	s_lshl_b32 s61, s49, 1
	s_add_u32 s60, s60, s61
	s_lshl_b32 s61, s58, 13
	s_lshl_b32 s62, s59, 8
	s_add_u32 s61, s61, s62
	s_add_u32 s66, s52, s61
	s_addc_u32 s67, s53, 0
	global_load_dword v214, v248, s[66:67]
	v_add_u32_e32 v248, 0x2000, v248
	global_load_dword v215, v248, s[66:67]
	v_add_u32_e32 v248, 0x2000, v248
	global_load_dword v216, v248, s[66:67]
	v_add_u32_e32 v248, 0x2000, v248
	global_load_dword v217, v248, s[66:67]
	v_add_u32_e32 v248, 0x2000, v248
	global_load_dword v218, v248, s[66:67]
	v_add_u32_e32 v248, 0x2000, v248
	global_load_dword v219, v248, s[66:67]
	v_add_u32_e32 v248, 0x2000, v248
	global_load_dword v220, v248, s[66:67]
	v_add_u32_e32 v248, 0x2000, v248
	global_load_dword v221, v248, s[66:67]
	v_add_u32_e32 v248, 0x2000, v248
	global_load_dword v222, v248, s[66:67]
	v_add_u32_e32 v248, 0x2000, v248
	global_load_dword v223, v248, s[66:67]
	v_add_u32_e32 v248, 0x2000, v248
	global_load_dword v224, v248, s[66:67]
	v_add_u32_e32 v248, 0x2000, v248
	global_load_dword v225, v248, s[66:67]
	v_add_u32_e32 v248, 0x2000, v248
	global_load_dword v226, v248, s[66:67]
	v_add_u32_e32 v248, 0x2000, v248
	global_load_dword v227, v248, s[66:67]
	v_add_u32_e32 v248, 0x2000, v248
	global_load_dword v228, v248, s[66:67]
	v_add_u32_e32 v248, 0x2000, v248
	global_load_dword v229, v248, s[66:67]
	v_add_u32_e32 v248, 0x2000, v248
	global_load_dword v230, v248, s[66:67]
	v_add_u32_e32 v248, 0x2000, v248
	global_load_dword v231, v248, s[66:67]
	v_add_u32_e32 v248, 0x2000, v248
	global_load_dword v232, v248, s[66:67]
	v_add_u32_e32 v248, 0x2000, v248
	global_load_dword v233, v248, s[66:67]
	v_add_u32_e32 v248, 0x2000, v248
	global_load_dword v234, v248, s[66:67]
	v_add_u32_e32 v248, 0x2000, v248
	global_load_dword v235, v248, s[66:67]
	v_add_u32_e32 v248, 0x2000, v248
	global_load_dword v236, v248, s[66:67]
	v_add_u32_e32 v248, 0x2000, v248
	global_load_dword v237, v248, s[66:67]
	v_add_u32_e32 v248, 0x2000, v248
	global_load_dword v238, v248, s[66:67]
	v_add_u32_e32 v248, 0x2000, v248
	global_load_dword v239, v248, s[66:67]
	v_add_u32_e32 v248, 0x2000, v248
	global_load_dword v240, v248, s[66:67]
	v_add_u32_e32 v248, 0x2000, v248
	global_load_dword v241, v248, s[66:67]
	v_add_u32_e32 v248, 0x2000, v248
	global_load_dword v242, v248, s[66:67]
	v_add_u32_e32 v248, 0x2000, v248
	global_load_dword v243, v248, s[66:67]
	v_add_u32_e32 v248, 0x2000, v248
	global_load_dword v244, v248, s[66:67]
	v_add_u32_e32 v248, 0x2000, v248
	global_load_dword v245, v248, s[66:67]
	v_add_u32_e32 v248, 0x2000, v248
	v_bitop3_b32 v153, v152, v14, v15 bitop3:0xf6
	s_waitcnt vmcnt(39) lgkmcnt(0)
	s_barrier
	ds_read_b128 v[42:45], v146
	ds_read_b128 v[38:41], v146 offset:2048
	ds_read_b128 v[10:13], v146 offset:4096
	ds_read_b128 v[6:9], v146 offset:6144
	ds_read_b128 v[22:25], v153 offset:32768
	ds_read_b128 v[18:21], v153 offset:34816
	ds_read_b128 v[30:33], v153 offset:36864
	ds_read_b128 v[26:29], v153 offset:38912
	ds_read_b128 v[34:37], v153 offset:40960
	ds_read_b128 v[14:17], v153 offset:43008
	v_lshl_or_b32 v2, v2, 15, v47
	v_lshl_or_b32 v2, v46, 11, v2
	v_lshl_add_u64 v[140:141], s[18:19], 0, v[2:3]
	v_lshl_add_u64 v[142:143], s[2:3], 0, v[2:3]
	s_mov_b32 s21, 0
	s_mov_b64 s[0:1], 0
	s_mov_b64 s[2:3], 0x100
	s_mov_b64 s[8:9], 0x20100
	s_mov_b64 s[16:17], 0x40100
	s_mov_b64 s[18:19], 0x60100
	v_mov_b32_e32 v2, v3
	v_mov_b32_e32 v4, v3
	v_mov_b32_e32 v5, v3
	v_mov_b32_e32 v46, v3
	v_mov_b32_e32 v47, v3
	v_mov_b32_e32 v48, v3
	v_mov_b32_e32 v49, v3
	v_mov_b32_e32 v50, v3
	v_mov_b32_e32 v51, v3
	v_mov_b32_e32 v52, v3
	v_mov_b32_e32 v53, v3
	v_mov_b32_e32 v54, v3
	v_mov_b32_e32 v55, v3
	v_mov_b32_e32 v56, v3
	v_mov_b32_e32 v57, v3
	v_mov_b32_e32 v58, v3
	v_mov_b32_e32 v59, v3
	v_mov_b32_e32 v60, v3
	v_mov_b32_e32 v61, v3
	v_mov_b32_e32 v62, v3
	v_mov_b32_e32 v63, v3
	v_mov_b32_e32 v64, v3
	v_mov_b32_e32 v65, v3
	v_mov_b32_e32 v66, v3
	v_mov_b32_e32 v67, v3
	v_mov_b32_e32 v68, v3
	v_mov_b32_e32 v69, v3
	v_mov_b32_e32 v70, v3
	v_mov_b32_e32 v71, v3
	v_mov_b32_e32 v72, v3
	v_mov_b32_e32 v73, v3
	v_mov_b32_e32 v74, v3
	v_mov_b32_e32 v75, v3
	v_mov_b32_e32 v76, v3
	v_mov_b32_e32 v77, v3
	v_mov_b32_e32 v86, v3
	v_mov_b32_e32 v87, v3
	v_mov_b32_e32 v88, v3
	v_mov_b32_e32 v89, v3
	v_mov_b32_e32 v98, v3
	v_mov_b32_e32 v99, v3
	v_mov_b32_e32 v100, v3
	v_mov_b32_e32 v101, v3
	v_mov_b32_e32 v130, v3
	v_mov_b32_e32 v131, v3
	v_mov_b32_e32 v132, v3
	v_mov_b32_e32 v133, v3
	v_mov_b32_e32 v78, v3
	v_mov_b32_e32 v79, v3
	v_mov_b32_e32 v80, v3
	v_mov_b32_e32 v81, v3
	v_mov_b32_e32 v82, v3
	v_mov_b32_e32 v83, v3
	v_mov_b32_e32 v84, v3
	v_mov_b32_e32 v85, v3
	v_mov_b32_e32 v90, v3
	v_mov_b32_e32 v91, v3
	v_mov_b32_e32 v92, v3
	v_mov_b32_e32 v93, v3
	v_mov_b32_e32 v94, v3
	v_mov_b32_e32 v95, v3
	v_mov_b32_e32 v96, v3
	v_mov_b32_e32 v97, v3
	v_mov_b32_e32 v102, v3
	v_mov_b32_e32 v103, v3
	v_mov_b32_e32 v104, v3
	v_mov_b32_e32 v105, v3
	v_mov_b32_e32 v106, v3
	v_mov_b32_e32 v107, v3
	v_mov_b32_e32 v108, v3
	v_mov_b32_e32 v109, v3
	v_mov_b32_e32 v110, v3
	v_mov_b32_e32 v111, v3
	v_mov_b32_e32 v112, v3
	v_mov_b32_e32 v113, v3
	v_mov_b32_e32 v114, v3
	v_mov_b32_e32 v115, v3
	v_mov_b32_e32 v116, v3
	v_mov_b32_e32 v117, v3
	v_mov_b32_e32 v118, v3
	v_mov_b32_e32 v119, v3
	v_mov_b32_e32 v120, v3
	v_mov_b32_e32 v121, v3
	v_mov_b32_e32 v122, v3
	v_mov_b32_e32 v123, v3
	v_mov_b32_e32 v124, v3
	v_mov_b32_e32 v125, v3
	v_mov_b32_e32 v134, v3
	v_mov_b32_e32 v135, v3
	v_mov_b32_e32 v136, v3
	v_mov_b32_e32 v137, v3
	v_mov_b32_e32 v126, v3
	v_mov_b32_e32 v127, v3
	v_mov_b32_e32 v128, v3
	v_mov_b32_e32 v129, v3
.LBB2_1:
	s_mul_i32 s22, s21, 0xe000
	v_add_u32_e32 v166, s22, v146
	v_add_u32_e32 v190, s22, v153
	s_waitcnt lgkmcnt(0)
	v_mfma_f32_16x16x32_f16 v[130:133], v[22:25], v[42:45], v[130:133]
	ds_read_b128 v[154:157], v166 offset:1024
	ds_read_b128 v[158:161], v166 offset:3072
	s_add_i32 s21, s21, 1
	v_mfma_f32_16x16x32_f16 v[98:101], v[18:21], v[42:45], v[98:101]
	ds_read_b128 v[162:165], v166 offset:5120
	ds_read_b128 v[166:169], v166 offset:7168
	v_mfma_f32_16x16x32_f16 v[86:89], v[30:33], v[42:45], v[86:89]
	ds_read_b128 v[170:173], v190 offset:33792
	ds_read_b128 v[174:177], v190 offset:35840
	v_mfma_f32_16x16x32_f16 v[74:77], v[26:29], v[42:45], v[74:77]
	ds_read_b128 v[178:181], v190 offset:37888
	ds_read_b128 v[182:185], v190 offset:39936
	v_mfma_f32_16x16x32_f16 v[70:73], v[42:45], v[34:37], v[70:73]
	ds_read_b128 v[186:189], v190 offset:41984
	ds_read_b128 v[190:193], v190 offset:44032
	v_mfma_f32_16x16x32_f16 v[66:69], v[42:45], v[14:17], v[66:69]
	v_mfma_f32_16x16x32_f16 v[62:65], v[22:25], v[38:41], v[62:65]
	v_mfma_f32_16x16x32_f16 v[58:61], v[18:21], v[38:41], v[58:61]
	v_mfma_f32_16x16x32_f16 v[54:57], v[30:33], v[38:41], v[54:57]
	v_mfma_f32_16x16x32_f16 v[50:53], v[26:29], v[38:41], v[50:53]
	v_mfma_f32_16x16x32_f16 v[46:49], v[38:41], v[34:37], v[46:49]
	v_mfma_f32_16x16x32_f16 v[2:5], v[38:41], v[14:17], v[2:5]
	v_mfma_f32_16x16x32_f16 v[78:81], v[22:25], v[10:13], v[78:81]
	v_mfma_f32_16x16x32_f16 v[82:85], v[18:21], v[10:13], v[82:85]
	v_mfma_f32_16x16x32_f16 v[90:93], v[30:33], v[10:13], v[90:93]
	v_mfma_f32_16x16x32_f16 v[94:97], v[26:29], v[10:13], v[94:97]
	v_mfma_f32_16x16x32_f16 v[102:105], v[10:13], v[34:37], v[102:105]
	v_mfma_f32_16x16x32_f16 v[106:109], v[10:13], v[14:17], v[106:109]
	v_mfma_f32_16x16x32_f16 v[110:113], v[22:25], v[6:9], v[110:113]
	v_mfma_f32_16x16x32_f16 v[114:117], v[18:21], v[6:9], v[114:117]
	v_mfma_f32_16x16x32_f16 v[118:121], v[30:33], v[6:9], v[118:121]
	v_mfma_f32_16x16x32_f16 v[122:125], v[26:29], v[6:9], v[122:125]
	v_mfma_f32_16x16x32_f16 v[134:137], v[6:9], v[34:37], v[134:137]
	v_mfma_f32_16x16x32_f16 v[126:129], v[6:9], v[14:17], v[126:129]
	v_or_b32_e32 v10, s22, v139
	v_lshl_add_u64 v[6:7], v[142:143], 0, s[0:1]
	v_readfirstlane_b32 s22, v10
	v_add_u32_e32 v11, 0x2000, v10
	v_lshl_add_u64 v[8:9], v[6:7], 0, s[2:3]
	s_mov_b32 m0, s22
	v_readfirstlane_b32 s22, v11
	v_add_u32_e32 v11, 0x4000, v10
	s_waitcnt vmcnt(0) lgkmcnt(0)
	s_barrier
	global_load_lds_dwordx4 v[8:9], off
	v_lshl_add_u64 v[8:9], v[6:7], 0, s[8:9]
	s_mov_b32 m0, s22
	v_readfirstlane_b32 s22, v11
	global_load_lds_dwordx4 v[8:9], off
	v_lshl_add_u64 v[8:9], v[6:7], 0, s[16:17]
	s_mov_b32 m0, s22
	v_lshl_add_u64 v[6:7], v[6:7], 0, s[18:19]
	global_load_lds_dwordx4 v[8:9], off
	v_add_u32_e32 v8, 0x6000, v10
	v_add_u32_e32 v11, 0x8000, v10
	v_readfirstlane_b32 s22, v8
	s_mov_b32 m0, s22
	v_readfirstlane_b32 s22, v11
	global_load_lds_dwordx4 v[6:7], off
	v_lshl_add_u64 v[6:7], v[140:141], 0, s[0:1]
	v_add_u32_e32 v11, 0xa000, v10
	v_lshl_add_u64 v[8:9], v[6:7], 0, s[2:3]
	s_mov_b32 m0, s22
	v_readfirstlane_b32 s22, v11
	global_load_lds_dwordx4 v[8:9], off
	v_lshl_add_u64 v[8:9], v[6:7], 0, s[8:9]
	s_mov_b32 m0, s22
	v_lshl_add_u64 v[6:7], v[6:7], 0, s[16:17]
	global_load_lds_dwordx4 v[8:9], off
	v_add_u32_e32 v8, 0xc000, v10
	s_cmp_lg_u32 s21, 2
	v_readfirstlane_b32 s22, v8
	s_mov_b32 m0, s22
	s_cselect_b32 s21, s21, 0
	global_load_lds_dwordx4 v[6:7], off
	s_mul_i32 s22, s21, 0xe000
	v_add_u32_e32 v6, s22, v146
	v_add_u32_e32 v14, s22, v153
	s_waitcnt lgkmcnt(0)
	v_mfma_f32_16x16x32_f16 v[130:133], v[170:173], v[154:157], v[130:133]
	ds_read_b128 v[42:45], v6
	ds_read_b128 v[38:41], v6 offset:2048
	v_mfma_f32_16x16x32_f16 v[98:101], v[174:177], v[154:157], v[98:101]
	ds_read_b128 v[10:13], v6 offset:4096
	ds_read_b128 v[6:9], v6 offset:6144
	v_mfma_f32_16x16x32_f16 v[86:89], v[178:181], v[154:157], v[86:89]
	ds_read_b128 v[22:25], v14 offset:32768
	ds_read_b128 v[18:21], v14 offset:34816
	v_mfma_f32_16x16x32_f16 v[74:77], v[182:185], v[154:157], v[74:77]
	ds_read_b128 v[30:33], v14 offset:36864
	ds_read_b128 v[26:29], v14 offset:38912
	v_mfma_f32_16x16x32_f16 v[70:73], v[154:157], v[186:189], v[70:73]
	ds_read_b128 v[34:37], v14 offset:40960
	ds_read_b128 v[14:17], v14 offset:43008
	v_mfma_f32_16x16x32_f16 v[66:69], v[154:157], v[190:193], v[66:69]
	v_mfma_f32_16x16x32_f16 v[62:65], v[170:173], v[158:161], v[62:65]
	v_mfma_f32_16x16x32_f16 v[58:61], v[174:177], v[158:161], v[58:61]
	v_mfma_f32_16x16x32_f16 v[54:57], v[178:181], v[158:161], v[54:57]
	v_mfma_f32_16x16x32_f16 v[50:53], v[182:185], v[158:161], v[50:53]
	v_mfma_f32_16x16x32_f16 v[46:49], v[158:161], v[186:189], v[46:49]
	v_mfma_f32_16x16x32_f16 v[2:5], v[158:161], v[190:193], v[2:5]
	v_mfma_f32_16x16x32_f16 v[78:81], v[170:173], v[162:165], v[78:81]
	v_mfma_f32_16x16x32_f16 v[82:85], v[174:177], v[162:165], v[82:85]
	v_mfma_f32_16x16x32_f16 v[90:93], v[178:181], v[162:165], v[90:93]
	v_mfma_f32_16x16x32_f16 v[94:97], v[182:185], v[162:165], v[94:97]
	v_mfma_f32_16x16x32_f16 v[102:105], v[162:165], v[186:189], v[102:105]
	v_mfma_f32_16x16x32_f16 v[106:109], v[162:165], v[190:193], v[106:109]
	v_mfma_f32_16x16x32_f16 v[110:113], v[170:173], v[166:169], v[110:113]
	v_mfma_f32_16x16x32_f16 v[114:117], v[174:177], v[166:169], v[114:117]
	v_mfma_f32_16x16x32_f16 v[118:121], v[178:181], v[166:169], v[118:121]
	v_mfma_f32_16x16x32_f16 v[122:125], v[182:185], v[166:169], v[122:125]
	v_mfma_f32_16x16x32_f16 v[134:137], v[166:169], v[186:189], v[134:137]
	v_mfma_f32_16x16x32_f16 v[126:129], v[166:169], v[190:193], v[126:129]
	s_add_u32 s0, s0, 0x80
	s_addc_u32 s1, s1, 0
	s_cmpk_eq_i32 s0, 0x700
	s_cbranch_scc0 .LBB2_1
	v_cmp_ne_u32_e64 s[68:69], 0, v214
	v_cmp_ne_u32_e64 s[70:71], 0, v215
	s_mov_b64 s[72:73], s[68:69]
	s_mov_b64 s[74:75], s[68:69]
	v_writelane_b32 v246, s68, 0
	v_writelane_b32 v247, s69, 0
	v_cmp_ne_u32_e64 s[68:69], 0, v216
	s_or_b64 s[72:73], s[72:73], s[70:71]
	s_and_b64 s[74:75], s[74:75], s[70:71]
	v_writelane_b32 v246, s70, 1
	v_writelane_b32 v247, s71, 1
	v_cmp_ne_u32_e64 s[70:71], 0, v217
	s_or_b64 s[72:73], s[72:73], s[68:69]
	s_and_b64 s[74:75], s[74:75], s[68:69]
	v_writelane_b32 v246, s68, 2
	v_writelane_b32 v247, s69, 2
	v_cmp_ne_u32_e64 s[68:69], 0, v218
	s_or_b64 s[72:73], s[72:73], s[70:71]
	s_and_b64 s[74:75], s[74:75], s[70:71]
	v_writelane_b32 v246, s70, 3
	v_writelane_b32 v247, s71, 3
	v_cmp_ne_u32_e64 s[70:71], 0, v219
	s_or_b64 s[72:73], s[72:73], s[68:69]
	s_and_b64 s[74:75], s[74:75], s[68:69]
	v_writelane_b32 v246, s68, 4
	v_writelane_b32 v247, s69, 4
	v_cmp_ne_u32_e64 s[68:69], 0, v220
	s_or_b64 s[72:73], s[72:73], s[70:71]
	s_and_b64 s[74:75], s[74:75], s[70:71]
	v_writelane_b32 v246, s70, 5
	v_writelane_b32 v247, s71, 5
	v_cmp_ne_u32_e64 s[70:71], 0, v221
	s_or_b64 s[72:73], s[72:73], s[68:69]
	s_and_b64 s[74:75], s[74:75], s[68:69]
	v_writelane_b32 v246, s68, 6
	v_writelane_b32 v247, s69, 6
	v_cmp_ne_u32_e64 s[68:69], 0, v222
	s_or_b64 s[72:73], s[72:73], s[70:71]
	s_and_b64 s[74:75], s[74:75], s[70:71]
	v_writelane_b32 v246, s70, 7
	v_writelane_b32 v247, s71, 7
	v_cmp_ne_u32_e64 s[70:71], 0, v223
	s_or_b64 s[72:73], s[72:73], s[68:69]
	s_and_b64 s[74:75], s[74:75], s[68:69]
	v_writelane_b32 v246, s68, 8
	v_writelane_b32 v247, s69, 8
	v_cmp_ne_u32_e64 s[68:69], 0, v224
	s_or_b64 s[72:73], s[72:73], s[70:71]
	s_and_b64 s[74:75], s[74:75], s[70:71]
	v_writelane_b32 v246, s70, 9
	v_writelane_b32 v247, s71, 9
	v_cmp_ne_u32_e64 s[70:71], 0, v225
	s_or_b64 s[72:73], s[72:73], s[68:69]
	s_and_b64 s[74:75], s[74:75], s[68:69]
	v_writelane_b32 v246, s68, 10
	v_writelane_b32 v247, s69, 10
	v_cmp_ne_u32_e64 s[68:69], 0, v226
	s_or_b64 s[72:73], s[72:73], s[70:71]
	s_and_b64 s[74:75], s[74:75], s[70:71]
	v_writelane_b32 v246, s70, 11
	v_writelane_b32 v247, s71, 11
	v_cmp_ne_u32_e64 s[70:71], 0, v227
	s_or_b64 s[72:73], s[72:73], s[68:69]
	s_and_b64 s[74:75], s[74:75], s[68:69]
	v_writelane_b32 v246, s68, 12
	v_writelane_b32 v247, s69, 12
	v_cmp_ne_u32_e64 s[68:69], 0, v228
	s_or_b64 s[72:73], s[72:73], s[70:71]
	s_and_b64 s[74:75], s[74:75], s[70:71]
	v_writelane_b32 v246, s70, 13
	v_writelane_b32 v247, s71, 13
	v_cmp_ne_u32_e64 s[70:71], 0, v229
	s_or_b64 s[72:73], s[72:73], s[68:69]
	s_and_b64 s[74:75], s[74:75], s[68:69]
	v_writelane_b32 v246, s68, 14
	v_writelane_b32 v247, s69, 14
	v_cmp_ne_u32_e64 s[68:69], 0, v230
	s_or_b64 s[72:73], s[72:73], s[70:71]
	s_and_b64 s[74:75], s[74:75], s[70:71]
	v_writelane_b32 v246, s70, 15
	v_writelane_b32 v247, s71, 15
	s_cmp_lg_u64 s[72:73], 0
	s_cselect_b32 s76, 1, 0
	s_cmp_eq_u64 s[74:75], -1
	s_cselect_b32 s78, 2, 0
	s_lshr_b64 s[80:81], s[72:73], 16
	s_cmp_eq_u64 s[80:81], 0
	s_cselect_b32 s79, 4, 0
	s_or_b32 s76, s76, s78
	s_or_b32 s76, s76, s79
	v_cmp_ne_u32_e64 s[70:71], 0, v231
	s_mov_b64 s[72:73], s[68:69]
	s_mov_b64 s[74:75], s[68:69]
	v_writelane_b32 v246, s68, 16
	v_writelane_b32 v247, s69, 16
	v_cmp_ne_u32_e64 s[68:69], 0, v232
	s_or_b64 s[72:73], s[72:73], s[70:71]
	s_and_b64 s[74:75], s[74:75], s[70:71]
	v_writelane_b32 v246, s70, 17
	v_writelane_b32 v247, s71, 17
	v_cmp_ne_u32_e64 s[70:71], 0, v233
	s_or_b64 s[72:73], s[72:73], s[68:69]
	s_and_b64 s[74:75], s[74:75], s[68:69]
	v_writelane_b32 v246, s68, 18
	v_writelane_b32 v247, s69, 18
	v_cmp_ne_u32_e64 s[68:69], 0, v234
	s_or_b64 s[72:73], s[72:73], s[70:71]
	s_and_b64 s[74:75], s[74:75], s[70:71]
	v_writelane_b32 v246, s70, 19
	v_writelane_b32 v247, s71, 19
	v_cmp_ne_u32_e64 s[70:71], 0, v235
	s_or_b64 s[72:73], s[72:73], s[68:69]
	s_and_b64 s[74:75], s[74:75], s[68:69]
	v_writelane_b32 v246, s68, 20
	v_writelane_b32 v247, s69, 20
	v_cmp_ne_u32_e64 s[68:69], 0, v236
	s_or_b64 s[72:73], s[72:73], s[70:71]
	s_and_b64 s[74:75], s[74:75], s[70:71]
	v_writelane_b32 v246, s70, 21
	v_writelane_b32 v247, s71, 21
	v_cmp_ne_u32_e64 s[70:71], 0, v237
	s_or_b64 s[72:73], s[72:73], s[68:69]
	s_and_b64 s[74:75], s[74:75], s[68:69]
	v_writelane_b32 v246, s68, 22
	v_writelane_b32 v247, s69, 22
	v_cmp_ne_u32_e64 s[68:69], 0, v238
	s_or_b64 s[72:73], s[72:73], s[70:71]
	s_and_b64 s[74:75], s[74:75], s[70:71]
	v_writelane_b32 v246, s70, 23
	v_writelane_b32 v247, s71, 23
	v_cmp_ne_u32_e64 s[70:71], 0, v239
	s_or_b64 s[72:73], s[72:73], s[68:69]
	s_and_b64 s[74:75], s[74:75], s[68:69]
	v_writelane_b32 v246, s68, 24
	v_writelane_b32 v247, s69, 24
	v_cmp_ne_u32_e64 s[68:69], 0, v240
	s_or_b64 s[72:73], s[72:73], s[70:71]
	s_and_b64 s[74:75], s[74:75], s[70:71]
	v_writelane_b32 v246, s70, 25
	v_writelane_b32 v247, s71, 25
	v_cmp_ne_u32_e64 s[70:71], 0, v241
	s_or_b64 s[72:73], s[72:73], s[68:69]
	s_and_b64 s[74:75], s[74:75], s[68:69]
	v_writelane_b32 v246, s68, 26
	v_writelane_b32 v247, s69, 26
	v_cmp_ne_u32_e64 s[68:69], 0, v242
	s_or_b64 s[72:73], s[72:73], s[70:71]
	s_and_b64 s[74:75], s[74:75], s[70:71]
	v_writelane_b32 v246, s70, 27
	v_writelane_b32 v247, s71, 27
	v_cmp_ne_u32_e64 s[70:71], 0, v243
	s_or_b64 s[72:73], s[72:73], s[68:69]
	s_and_b64 s[74:75], s[74:75], s[68:69]
	v_writelane_b32 v246, s68, 28
	v_writelane_b32 v247, s69, 28
	v_cmp_ne_u32_e64 s[68:69], 0, v244
	s_or_b64 s[72:73], s[72:73], s[70:71]
	s_and_b64 s[74:75], s[74:75], s[70:71]
	v_writelane_b32 v246, s70, 29
	v_writelane_b32 v247, s71, 29
	v_cmp_ne_u32_e64 s[70:71], 0, v245
	s_or_b64 s[72:73], s[72:73], s[68:69]
	s_and_b64 s[74:75], s[74:75], s[68:69]
	v_writelane_b32 v246, s68, 30
	v_writelane_b32 v247, s69, 30
	s_nop 1
	s_or_b64 s[72:73], s[72:73], s[70:71]
	s_and_b64 s[74:75], s[74:75], s[70:71]
	v_writelane_b32 v246, s70, 31
	v_writelane_b32 v247, s71, 31
	s_cmp_lg_u64 s[72:73], 0
	s_cselect_b32 s77, 1, 0
	s_cmp_eq_u64 s[74:75], -1
	s_cselect_b32 s78, 2, 0
	s_lshr_b64 s[80:81], s[72:73], 16
	s_cmp_eq_u64 s[80:81], 0
	s_cselect_b32 s79, 4, 0
	s_or_b32 s77, s77, s78
	s_or_b32 s77, s77, s79
	v_and_b32_e32 v248, 63, v0
	v_lshlrev_b32_e32 v248, 3, v248
	s_lshl_b32 s84, s59, 11
	s_add_u32 s84, s84, s58
	s_lshl_b32 s84, s84, 3
	s_add_u32 s82, s54, s84
	s_addc_u32 s83, s55, 0
	v_mov_b32_e32 v249, s76
	v_mov_b32_e32 v251, s77
	v_mov_b32_e32 v250, s60
	v_add_u32_e32 v252, 1, v250
	s_mov_b32 exec_hi, 0
	global_store_dwordx2 v248, v[246:247], s[82:83]
	s_mov_b32 exec_lo, 1
	global_store_byte v250, v249, s[56:57]
	global_store_byte v252, v251, s[56:57]
	s_mov_b64 exec, -1
	s_nop 4
	s_waitcnt lgkmcnt(0)
	v_mfma_f32_16x16x32_f16 v[130:133], v[22:25], v[42:45], v[130:133]
	ds_read_b128 v[140:143], v146 offset:1024
	ds_read_b128 v[154:157], v146 offset:3072
	v_mfma_f32_16x16x32_f16 v[98:101], v[18:21], v[42:45], v[98:101]
	ds_read_b128 v[158:161], v146 offset:5120
	ds_read_b128 v[162:165], v146 offset:7168
	v_mfma_f32_16x16x32_f16 v[86:89], v[30:33], v[42:45], v[86:89]
	ds_read_b128 v[166:169], v153 offset:33792
	ds_read_b128 v[170:173], v153 offset:35840
	v_mfma_f32_16x16x32_f16 v[74:77], v[26:29], v[42:45], v[74:77]
	ds_read_b128 v[174:177], v153 offset:37888
	ds_read_b128 v[178:181], v153 offset:39936
	v_mfma_f32_16x16x32_f16 v[70:73], v[42:45], v[34:37], v[70:73]
	ds_read_b128 v[182:185], v153 offset:41984
	ds_read_b128 v[186:189], v153 offset:44032
	v_mfma_f32_16x16x32_f16 v[42:45], v[42:45], v[14:17], v[66:69]
	v_mfma_f32_16x16x32_f16 v[62:65], v[22:25], v[38:41], v[62:65]
	v_mfma_f32_16x16x32_f16 v[58:61], v[18:21], v[38:41], v[58:61]
	v_mfma_f32_16x16x32_f16 v[54:57], v[30:33], v[38:41], v[54:57]
	v_mfma_f32_16x16x32_f16 v[50:53], v[26:29], v[38:41], v[50:53]
	v_mfma_f32_16x16x32_f16 v[46:49], v[38:41], v[34:37], v[46:49]
	v_mfma_f32_16x16x32_f16 v[2:5], v[38:41], v[14:17], v[2:5]
	v_mfma_f32_16x16x32_f16 v[38:41], v[22:25], v[10:13], v[78:81]
	v_mfma_f32_16x16x32_f16 v[66:69], v[18:21], v[10:13], v[82:85]
	v_mfma_f32_16x16x32_f16 v[78:81], v[30:33], v[10:13], v[90:93]
	v_mfma_f32_16x16x32_f16 v[82:85], v[26:29], v[10:13], v[94:97]
	v_mfma_f32_16x16x32_f16 v[90:93], v[10:13], v[34:37], v[102:105]
	v_mfma_f32_16x16x32_f16 v[94:97], v[10:13], v[14:17], v[106:109]
	v_mfma_f32_16x16x32_f16 v[22:25], v[22:25], v[6:9], v[110:113]
	v_mfma_f32_16x16x32_f16 v[102:105], v[18:21], v[6:9], v[114:117]
	v_or_b32_e32 v21, v151, v152
	v_and_b32_e32 v20, 63, v0
	v_mfma_f32_16x16x32_f16 v[30:33], v[30:33], v[6:9], v[118:121]
	v_mfma_f32_16x16x32_f16 v[26:29], v[26:29], v[6:9], v[122:125]
	v_mfma_f32_16x16x32_f16 v[34:37], v[6:9], v[34:37], v[134:137]
	v_mfma_f32_16x16x32_f16 v[6:9], v[6:9], v[14:17], v[126:129]
	v_add_u32_e32 v10, 0x16800, v21
	s_waitcnt vmcnt(0) lgkmcnt(0)
	s_waitcnt lgkmcnt(0)
	v_mfma_f32_16x16x32_f16 v[16:19], v[166:169], v[140:143], v[130:133]
	s_barrier
	ds_read_b128 v[106:109], v146 offset:57344
	ds_read_b128 v[110:113], v146 offset:59392
	v_mfma_f32_16x16x32_f16 v[98:101], v[170:173], v[140:143], v[98:101]
	ds_read_b128 v[114:117], v146 offset:61440
	ds_read_b128 v[12:15], v146 offset:63488
	v_add_u32_e32 v0, 0x16000, v21
	v_mfma_f32_16x16x32_f16 v[86:89], v[174:177], v[140:143], v[86:89]
	ds_read_b128 v[122:125], v10
	v_add_u32_e32 v10, 0x17000, v21
	ds_read_b128 v[118:121], v0
	v_mfma_f32_16x16x32_f16 v[74:77], v[178:181], v[140:143], v[74:77]
	ds_read_b128 v[126:129], v10
	v_add_u32_e32 v10, 0x17800, v21
	ds_read_b128 v[130:133], v10
	v_mfma_f32_16x16x32_f16 v[70:73], v[140:143], v[182:185], v[70:73]
	ds_read_b128 v[134:137], v0 offset:8192
	ds_read_b128 v[190:193], v0 offset:10240
	v_mfma_f32_16x16x32_f16 v[42:45], v[140:143], v[186:189], v[42:45]
	v_mfma_f32_16x16x32_f16 v[62:65], v[166:169], v[154:157], v[62:65]
	v_mfma_f32_16x16x32_f16 v[58:61], v[170:173], v[154:157], v[58:61]
	v_mfma_f32_16x16x32_f16 v[54:57], v[174:177], v[154:157], v[54:57]
	v_mfma_f32_16x16x32_f16 v[50:53], v[178:181], v[154:157], v[50:53]
	v_mfma_f32_16x16x32_f16 v[46:49], v[154:157], v[182:185], v[46:49]
	v_mfma_f32_16x16x32_f16 v[140:143], v[154:157], v[186:189], v[2:5]
	v_mfma_f32_16x16x32_f16 v[38:41], v[166:169], v[158:161], v[38:41]
	v_mfma_f32_16x16x32_f16 v[66:69], v[170:173], v[158:161], v[66:69]
	v_mfma_f32_16x16x32_f16 v[78:81], v[174:177], v[158:161], v[78:81]
	v_mfma_f32_16x16x32_f16 v[82:85], v[178:181], v[158:161], v[82:85]
	v_mfma_f32_16x16x32_f16 v[90:93], v[158:161], v[182:185], v[90:93]
	v_mfma_f32_16x16x32_f16 v[94:97], v[158:161], v[186:189], v[94:97]
	v_mfma_f32_16x16x32_f16 v[22:25], v[166:169], v[162:165], v[22:25]
	v_mfma_f32_16x16x32_f16 v[102:105], v[170:173], v[162:165], v[102:105]
	v_mfma_f32_16x16x32_f16 v[30:33], v[174:177], v[162:165], v[30:33]
	v_mfma_f32_16x16x32_f16 v[26:29], v[178:181], v[162:165], v[26:29]
	v_mfma_f32_16x16x32_f16 v[34:37], v[162:165], v[182:185], v[34:37]
	v_mfma_f32_16x16x32_f16 v[152:155], v[162:165], v[186:189], v[6:9]
	s_waitcnt lgkmcnt(0)
	v_mfma_f32_16x16x32_f16 v[156:159], v[118:121], v[106:109], v[16:19]
	s_movk_i32 s0, 0x7c0
	ds_read_b128 v[202:205], v0 offset:9216
	ds_read_b128 v[206:209], v0 offset:11264
	v_lshlrev_b32_e32 v16, 6, v144
	v_mov_b32_e32 v17, 0
	v_mov_b32_e32 v139, v17
	v_lshl_add_u64 v[4:5], s[6:7], 0, v[16:17]
	v_lshl_add_u64 v[8:9], v[4:5], 0, v[138:139]
	s_waitcnt vmcnt(0)
	v_lshlrev_b32_e32 v4, 5, v150
	v_lshl_add_u64 v[2:3], s[4:5], 0, v[16:17]
	v_ashrrev_i32_e32 v5, 31, v4
	v_lshl_add_u64 v[2:3], v[2:3], 0, v[138:139]
	v_lshlrev_b64 v[4:5], 2, v[4:5]
	v_lshl_add_u64 v[6:7], v[2:3], 0, v[4:5]
	v_lshl_add_u64 v[4:5], v[8:9], 0, v[4:5]
	v_mfma_f32_16x16x32_f16 v[98:101], v[122:125], v[106:109], v[98:101]
	global_load_dwordx4 v[160:163], v[6:7], off
	v_lshlrev_b32_e32 v18, 5, v147
	v_ashrrev_i32_e32 v19, 31, v18
	v_mfma_f32_16x16x32_f16 v[86:89], v[126:129], v[106:109], v[86:89]
	v_lshlrev_b64 v[18:19], 2, v[18:19]
	ds_read_b128 v[172:175], v146 offset:62464
	ds_read_b128 v[176:179], v146 offset:64512
	v_mfma_f32_16x16x32_f16 v[74:77], v[130:133], v[106:109], v[74:77]
	v_mfma_f32_16x16x32_f16 v[70:73], v[106:109], v[134:137], v[70:73]
	v_mfma_f32_16x16x32_f16 v[42:45], v[106:109], v[190:193], v[42:45]
	global_load_dwordx4 v[106:109], v[4:5], off
	v_lshlrev_b32_e32 v4, 5, v149
	v_ashrrev_i32_e32 v5, 31, v4
	v_lshlrev_b64 v[4:5], 2, v[4:5]
	v_lshl_add_u64 v[6:7], v[2:3], 0, v[4:5]
	v_lshl_add_u64 v[4:5], v[8:9], 0, v[4:5]
	global_load_dwordx4 v[168:171], v[4:5], off
	global_load_dwordx4 v[164:167], v[6:7], off
	v_lshlrev_b32_e32 v4, 5, v148
	v_ashrrev_i32_e32 v5, 31, v4
	v_lshlrev_b64 v[10:11], 2, v[4:5]
	v_lshl_add_u64 v[4:5], v[2:3], 0, v[10:11]
	v_lshl_add_u64 v[10:11], v[8:9], 0, v[10:11]
	global_load_dwordx4 v[210:213], v[10:11], off
	v_lshl_add_u64 v[2:3], v[2:3], 0, v[18:19]
	global_load_dwordx4 v[4:7], v[4:5], off
	v_lshl_add_u64 v[8:9], v[8:9], 0, v[18:19]
	v_add_u32_e32 v18, 0x16400, v21
	v_ashrrev_i32_e32 v10, 7, v145
	ds_read_b128 v[180:183], v18
	v_add_u32_e32 v18, 0x17400, v21
	v_and_b32_e32 v10, -16, v10
	v_add_u32_e32 v19, 0x16c00, v21
	ds_read_b128 v[194:197], v18
	v_add_u32_e32 v18, s20, v10
	global_load_dwordx4 v[8:11], v[8:9], off
	ds_read_b128 v[184:187], v19
	v_add_u32_e32 v19, 0x17c00, v21
	v_and_or_b32 v21, v145, s0, v1
	global_load_dwordx4 v[0:3], v[2:3], off
	v_mfma_f32_16x16x32_f16 v[62:65], v[118:121], v[110:113], v[62:65]
	ds_read_b128 v[198:201], v19
	v_ashrrev_i32_e32 v19, 31, v18
	ds_read_b128 v[148:151], v146 offset:60416
	v_mfma_f32_16x16x32_f16 v[58:61], v[122:125], v[110:113], v[58:61]
	v_mfma_f32_16x16x32_f16 v[54:57], v[126:129], v[110:113], v[54:57]
	v_mfma_f32_16x16x32_f16 v[50:53], v[130:133], v[110:113], v[50:53]
	v_mfma_f32_16x16x32_f16 v[46:49], v[110:113], v[134:137], v[46:49]
	v_mfma_f32_16x16x32_f16 v[110:113], v[110:113], v[190:193], v[140:143]
	s_nop 2
	ds_read_b128 v[140:143], v146 offset:58368
	v_mfma_f32_16x16x32_f16 v[38:41], v[118:121], v[114:117], v[38:41]
	v_mfma_f32_16x16x32_f16 v[66:69], v[122:125], v[114:117], v[66:69]
	v_mfma_f32_16x16x32_f16 v[78:81], v[126:129], v[114:117], v[78:81]
	v_mfma_f32_16x16x32_f16 v[82:85], v[130:133], v[114:117], v[82:85]
	v_mfma_f32_16x16x32_f16 v[90:93], v[114:117], v[134:137], v[90:93]
	v_mfma_f32_16x16x32_f16 v[94:97], v[114:117], v[190:193], v[94:97]
	s_waitcnt lgkmcnt(0)
	v_mfma_f32_16x16x32_f16 v[114:117], v[180:183], v[140:143], v[156:159]
	v_mfma_f32_16x16x32_f16 v[98:101], v[184:187], v[140:143], v[98:101]
	v_mfma_f32_16x16x32_f16 v[22:25], v[118:121], v[12:15], v[22:25]
	s_waitcnt vmcnt(6)
	s_nop 4
	v_pk_mul_f32 v[120:121], v[114:115], v[106:107] op_sel_hi:[1,0]
	v_lshlrev_b64 v[118:119], 17, v[18:19]
	v_lshl_or_b32 v118, v21, 6, v118
	v_mfma_f32_16x16x32_f16 v[102:105], v[122:125], v[12:15], v[102:105]
	v_mul_f32_e64 v122, v116, v107
	v_mul_f32_e64 v123, v117, v107
	v_pk_fma_f32 v[124:125], v[114:115], v[160:161], v[120:121] op_sel:[0,0,1] op_sel_hi:[1,1,0] neg_lo:[0,0,1] neg_hi:[0,0,1]
	v_pk_fma_f32 v[114:115], v[114:115], v[160:161], v[120:121] op_sel:[0,0,1] op_sel_hi:[1,0,0]
	v_pk_fma_f32 v[120:121], v[116:117], v[160:161], v[122:123] op_sel:[0,1,1] op_sel_hi:[1,1,0] neg_lo:[0,0,1] neg_hi:[0,0,1]
	v_pk_fma_f32 v[116:117], v[116:117], v[160:161], v[122:123] op_sel:[0,1,1] op_sel_hi:[1,1,0]
	v_cvt_pk_f16_f32 v114, v124, v115
	v_cvt_pk_f16_f32 v115, v120, v117
	v_pk_mul_f32 v[116:117], v[98:99], v[108:109] op_sel_hi:[1,0]
	v_mov_b32_e32 v122, v163
	v_pk_fma_f32 v[120:121], v[98:99], v[162:163], v[116:117] op_sel:[0,0,1] op_sel_hi:[1,1,0] neg_lo:[0,0,1] neg_hi:[0,0,1]
	v_pk_fma_f32 v[98:99], v[98:99], v[162:163], v[116:117] op_sel:[0,0,1] op_sel_hi:[1,0,0]
	v_mfma_f32_16x16x32_f16 v[30:33], v[126:129], v[12:15], v[30:33]
	v_cvt_pk_f16_f32 v116, v120, v99
	v_mov_b32_e32 v120, v109
	v_pk_mul_f32 v[98:99], v[100:101], v[120:121] op_sel_hi:[1,0]
	v_mfma_f32_16x16x32_f16 v[26:29], v[130:133], v[12:15], v[26:29]
	v_fma_f32 v124, v100, v122, -v99
	v_fma_f32 v125, v101, v122, -v98
	v_pk_fma_f32 v[98:99], v[100:101], v[122:123], v[98:99] op_sel:[0,0,1] op_sel_hi:[1,0,0]
	s_nop 0
	v_cvt_pk_f16_f32 v117, v124, v99
	v_lshlrev_b64 v[124:125], 1, v[118:119]
	v_lshl_add_u64 v[126:127], s[10:11], 0, v[124:125]
	v_mfma_f32_16x16x32_f16 v[34:37], v[12:15], v[134:137], v[34:37]
	v_mfma_f32_16x16x32_f16 v[98:101], v[12:15], v[190:193], v[152:155]
	v_lshl_add_u64 v[12:13], v[126:127], 0, v[16:17]
	v_lshl_add_u64 v[126:127], v[12:13], 0, v[138:139]
	global_store_dwordx4 v[126:127], v[114:117], off sc1
	v_mfma_f32_16x16x32_f16 v[12:15], v[194:197], v[140:143], v[86:89]
	v_mfma_f32_16x16x32_f16 v[74:77], v[198:201], v[140:143], v[74:77]
	v_mfma_f32_16x16x32_f16 v[58:61], v[184:187], v[148:151], v[58:61]
	s_nop 5
	v_mul_f32_e64 v86, v12, v106
	v_mul_f32_e64 v87, v13, v106
	v_pk_fma_f32 v[88:89], v[12:13], v[160:161], v[86:87] op_sel:[0,0,1] op_sel_hi:[1,1,0] neg_lo:[0,0,1] neg_hi:[0,0,1]
	v_pk_fma_f32 v[12:13], v[12:13], v[160:161], v[86:87] op_sel:[0,0,1] op_sel_hi:[1,0,0]
	v_mfma_f32_16x16x32_f16 v[54:57], v[194:197], v[148:151], v[54:57]
	v_cvt_pk_f16_f32 v86, v88, v13
	v_pk_mul_f32 v[12:13], v[14:15], v[106:107] op_sel:[0,1]
	s_nop 0
	v_pk_fma_f32 v[88:89], v[14:15], v[160:161], v[12:13] op_sel:[0,1,1] op_sel_hi:[1,1,0] neg_lo:[0,0,1] neg_hi:[0,0,1]
	v_pk_fma_f32 v[12:13], v[14:15], v[160:161], v[12:13] op_sel:[0,1,1] op_sel_hi:[1,1,0]
	v_mfma_f32_16x16x32_f16 v[50:53], v[198:201], v[148:151], v[50:53]
	v_cvt_pk_f16_f32 v87, v88, v13
	v_pk_mul_f32 v[88:89], v[74:75], v[108:109] op_sel_hi:[1,0]
	v_mfma_f32_16x16x32_f16 v[12:15], v[140:143], v[206:209], v[42:45]
	s_nop 2
	v_fma_f32 v42, v74, v162, -v89
	v_fma_f32 v43, v75, v163, -v88
	v_pk_fma_f32 v[44:45], v[74:75], v[162:163], v[88:89] op_sel:[0,0,1] op_sel_hi:[1,0,0]
	v_mfma_f32_16x16x32_f16 v[38:41], v[180:183], v[172:175], v[38:41]
	v_cvt_pk_f16_f32 v88, v42, v45
	v_mfma_f32_16x16x32_f16 v[42:45], v[180:183], v[148:151], v[62:65]
	s_nop 2
	v_mul_f32_e64 v62, v76, v120
	v_mul_f32_e64 v63, v77, v120
	v_mfma_f32_16x16x32_f16 v[66:69], v[184:187], v[172:175], v[66:69]
	v_fma_f32 v64, v76, v122, -v63
	v_fma_f32 v65, v77, v122, -v62
	v_pk_fma_f32 v[62:63], v[76:77], v[122:123], v[62:63] op_sel:[0,0,1] op_sel_hi:[1,0,0]
	s_nop 0
	v_cvt_pk_f16_f32 v89, v64, v63
	v_lshl_add_u64 v[62:63], s[12:13], 0, v[124:125]
	v_lshl_add_u64 v[62:63], v[62:63], 0, v[16:17]
	v_lshl_add_u64 v[106:107], v[62:63], 0, v[138:139]
	s_waitcnt vmcnt(6)
	v_pk_mul_f32 v[62:63], v[42:43], v[168:169] op_sel_hi:[1,0]
	global_store_dwordx4 v[106:107], v[86:89], off sc1
	s_waitcnt vmcnt(6)
	v_pk_fma_f32 v[64:65], v[42:43], v[164:165], v[62:63] op_sel:[0,0,1] op_sel_hi:[1,1,0] neg_lo:[0,0,1] neg_hi:[0,0,1]
	v_pk_fma_f32 v[42:43], v[42:43], v[164:165], v[62:63] op_sel:[0,0,1] op_sel_hi:[1,0,0]
	v_pk_mul_f32 v[62:63], v[44:45], v[168:169] op_sel:[0,1]
	v_cvt_pk_f16_f32 v42, v64, v43
	v_pk_fma_f32 v[74:75], v[44:45], v[164:165], v[62:63] op_sel:[0,1,1] op_sel_hi:[1,1,0] neg_lo:[0,0,1] neg_hi:[0,0,1]
	v_pk_fma_f32 v[44:45], v[44:45], v[164:165], v[62:63] op_sel:[0,1,1] op_sel_hi:[1,1,0]
	v_mov_b32_e32 v86, v171
	v_cvt_pk_f16_f32 v43, v74, v45
	v_pk_mul_f32 v[44:45], v[58:59], v[170:171] op_sel_hi:[1,0]
	v_mov_b32_e32 v88, v167
	v_pk_fma_f32 v[74:75], v[58:59], v[166:167], v[44:45] op_sel:[0,0,1] op_sel_hi:[1,1,0] neg_lo:[0,0,1] neg_hi:[0,0,1]
	v_pk_fma_f32 v[44:45], v[58:59], v[166:167], v[44:45] op_sel:[0,0,1] op_sel_hi:[1,0,0]
	v_pk_mul_f32 v[58:59], v[60:61], v[86:87] op_sel_hi:[1,0]
	v_cvt_pk_f16_f32 v44, v74, v45
	v_pk_fma_f32 v[108:109], v[60:61], v[88:89], v[58:59] op_sel:[0,0,1] op_sel_hi:[1,0,0] neg_lo:[0,0,1] neg_hi:[0,0,1]
	v_pk_fma_f32 v[58:59], v[60:61], v[88:89], v[58:59] op_sel:[0,0,1] op_sel_hi:[1,0,0]
	v_mfma_f32_16x16x32_f16 v[74:77], v[194:197], v[172:175], v[78:81]
	v_cvt_pk_f16_f32 v45, v108, v59
	global_store_dwordx4 v[126:127], v[42:45], off offset:2048 sc1
	v_pk_mul_f32 v[58:59], v[54:55], v[168:169] op_sel_hi:[1,0]
	v_mfma_f32_16x16x32_f16 v[22:25], v[180:183], v[176:179], v[22:25]
	v_fma_f32 v78, v54, v164, -v59
	v_fma_f32 v79, v55, v165, -v58
	v_pk_fma_f32 v[54:55], v[54:55], v[164:165], v[58:59] op_sel:[0,0,1] op_sel_hi:[1,0,0]
	v_mfma_f32_16x16x32_f16 v[42:45], v[198:201], v[172:175], v[82:85]
	v_cvt_pk_f16_f32 v54, v78, v55
	s_nop 1
	v_pk_mul_f32 v[82:83], v[56:57], v[168:169] op_sel:[0,1]
	v_mfma_f32_16x16x32_f16 v[30:33], v[194:197], v[176:179], v[30:33]
	v_fma_f32 v84, v56, v165, -v83
	v_fma_f32 v85, v57, v165, -v82
	v_pk_fma_f32 v[56:57], v[56:57], v[164:165], v[82:83] op_sel:[0,1,1] op_sel_hi:[1,1,0]
	s_nop 0
	v_cvt_pk_f16_f32 v55, v84, v57
	v_pk_mul_f32 v[56:57], v[50:51], v[170:171] op_sel_hi:[1,0]
	v_mfma_f32_16x16x32_f16 v[26:29], v[198:201], v[176:179], v[26:29]
	v_fma_f32 v82, v50, v166, -v57
	v_fma_f32 v83, v51, v167, -v56
	v_pk_fma_f32 v[50:51], v[50:51], v[166:167], v[56:57] op_sel:[0,0,1] op_sel_hi:[1,0,0]
	s_nop 0
	v_cvt_pk_f16_f32 v56, v82, v51
	v_pk_mul_f32 v[50:51], v[52:53], v[86:87] op_sel_hi:[1,0]
	v_mfma_f32_16x16x32_f16 v[82:85], v[184:187], v[176:179], v[102:105]
	v_fma_f32 v86, v52, v88, -v51
	v_fma_f32 v87, v53, v88, -v50
	v_pk_fma_f32 v[50:51], v[52:53], v[88:89], v[50:51] op_sel:[0,0,1] op_sel_hi:[1,0,0]
	s_nop 0
	v_cvt_pk_f16_f32 v57, v86, v51
	global_store_dwordx4 v[106:107], v[54:57], off offset:2048 sc1
	s_waitcnt vmcnt(7)
	v_pk_mul_f32 v[50:51], v[38:39], v[210:211] op_sel_hi:[1,0]
	v_mfma_f32_16x16x32_f16 v[70:73], v[140:143], v[202:205], v[70:73]
	v_mul_f32_e64 v56, v40, v211
	v_mul_f32_e64 v57, v41, v211
	s_waitcnt vmcnt(6)
	v_pk_fma_f32 v[52:53], v[38:39], v[4:5], v[50:51] op_sel:[0,0,1] op_sel_hi:[1,1,0] neg_lo:[0,0,1] neg_hi:[0,0,1]
	v_pk_fma_f32 v[38:39], v[38:39], v[4:5], v[50:51] op_sel:[0,0,1] op_sel_hi:[1,0,0]
	v_pk_fma_f32 v[86:87], v[40:41], v[4:5], v[56:57] op_sel:[0,1,1] op_sel_hi:[1,1,0] neg_lo:[0,0,1] neg_hi:[0,0,1]
	v_pk_fma_f32 v[40:41], v[40:41], v[4:5], v[56:57] op_sel:[0,1,1] op_sel_hi:[1,1,0]
	v_cvt_pk_f16_f32 v38, v52, v39
	v_cvt_pk_f16_f32 v39, v86, v41
	v_pk_mul_f32 v[40:41], v[66:67], v[212:213] op_sel_hi:[1,0]
	v_or_b32_e32 v54, 0x800, v118
	v_pk_fma_f32 v[56:57], v[66:67], v[6:7], v[40:41] op_sel:[0,0,1] op_sel_hi:[1,1,0] neg_lo:[0,0,1] neg_hi:[0,0,1]
	v_pk_fma_f32 v[40:41], v[66:67], v[6:7], v[40:41] op_sel:[0,0,1] op_sel_hi:[1,0,0]
	v_mov_b32_e32 v55, v119
	v_cvt_pk_f16_f32 v40, v56, v41
	v_mov_b32_e32 v56, v213
	v_pk_mul_f32 v[66:67], v[68:69], v[56:57] op_sel_hi:[1,0]
	v_mov_b32_e32 v86, v7
	v_pk_fma_f32 v[88:89], v[68:69], v[86:87], v[66:67] op_sel:[0,0,1] op_sel_hi:[1,0,0] neg_lo:[0,0,1] neg_hi:[0,0,1]
	v_pk_fma_f32 v[66:67], v[68:69], v[86:87], v[66:67] op_sel:[0,0,1] op_sel_hi:[1,0,0]
	v_lshlrev_b64 v[54:55], 1, v[54:55]
	v_cvt_pk_f16_f32 v41, v88, v67
	v_lshl_add_u64 v[66:67], s[10:11], 0, v[54:55]
	v_lshl_add_u64 v[66:67], v[66:67], 0, v[16:17]
	v_lshl_add_u64 v[66:67], v[66:67], 0, v[138:139]
	global_store_dwordx4 v[66:67], v[38:41], off sc1
	v_or_b32_e32 v118, 0xc00, v118
	v_mfma_f32_16x16x32_f16 v[46:49], v[148:151], v[202:205], v[46:49]
	v_mul_f32_e64 v38, v74, v210
	v_mul_f32_e64 v39, v75, v210
	v_pk_fma_f32 v[40:41], v[74:75], v[4:5], v[38:39] op_sel:[0,0,1] op_sel_hi:[1,1,0] neg_lo:[0,0,1] neg_hi:[0,0,1]
	v_pk_fma_f32 v[38:39], v[74:75], v[4:5], v[38:39] op_sel:[0,0,1] op_sel_hi:[1,0,0]
	v_mfma_f32_16x16x32_f16 v[58:61], v[172:175], v[202:205], v[90:93]
	v_cvt_pk_f16_f32 v38, v40, v39
	v_pk_mul_f32 v[40:41], v[76:77], v[210:211] op_sel:[0,1]
	s_nop 0
	v_pk_fma_f32 v[66:67], v[76:77], v[4:5], v[40:41] op_sel:[0,1,1] op_sel_hi:[1,1,0] neg_lo:[0,0,1] neg_hi:[0,0,1]
	v_pk_fma_f32 v[4:5], v[76:77], v[4:5], v[40:41] op_sel:[0,1,1] op_sel_hi:[1,1,0]
	v_mfma_f32_16x16x32_f16 v[34:37], v[176:179], v[202:205], v[34:37]
	v_cvt_pk_f16_f32 v39, v66, v5
	v_pk_mul_f32 v[4:5], v[42:43], v[212:213] op_sel_hi:[1,0]
	s_nop 0
	v_pk_fma_f32 v[40:41], v[42:43], v[6:7], v[4:5] op_sel:[0,0,1] op_sel_hi:[1,1,0] neg_lo:[0,0,1] neg_hi:[0,0,1]
	v_pk_fma_f32 v[4:5], v[42:43], v[6:7], v[4:5] op_sel:[0,0,1] op_sel_hi:[1,0,0]
	v_mfma_f32_16x16x32_f16 v[62:65], v[148:151], v[206:209], v[110:113]
	v_cvt_pk_f16_f32 v40, v40, v5
	v_pk_mul_f32 v[4:5], v[44:45], v[56:57] op_sel_hi:[1,0]
	s_nop 0
	v_pk_fma_f32 v[6:7], v[44:45], v[86:87], v[4:5] op_sel:[0,0,1] op_sel_hi:[1,0,0] neg_lo:[0,0,1] neg_hi:[0,0,1]
	v_pk_fma_f32 v[4:5], v[44:45], v[86:87], v[4:5] op_sel:[0,0,1] op_sel_hi:[1,0,0]
	v_mfma_f32_16x16x32_f16 v[78:81], v[172:175], v[206:209], v[94:97]
	v_cvt_pk_f16_f32 v41, v6, v5
	v_lshl_add_u64 v[4:5], s[12:13], 0, v[54:55]
	v_lshl_add_u64 v[4:5], v[4:5], 0, v[16:17]
	v_lshl_add_u64 v[4:5], v[4:5], 0, v[138:139]
	global_store_dwordx4 v[4:5], v[38:41], off sc1
	s_waitcnt vmcnt(7)
	v_pk_mul_f32 v[4:5], v[22:23], v[8:9] op_sel_hi:[1,0]
	v_mfma_f32_16x16x32_f16 v[50:53], v[176:179], v[206:209], v[98:101]
	s_waitcnt vmcnt(6)
	v_pk_fma_f32 v[6:7], v[22:23], v[0:1], v[4:5] op_sel:[0,0,1] op_sel_hi:[1,1,0] neg_lo:[0,0,1] neg_hi:[0,0,1]
	v_pk_fma_f32 v[4:5], v[22:23], v[0:1], v[4:5] op_sel:[0,0,1] op_sel_hi:[1,0,0]
	v_mov_b32_e32 v38, v3
	v_cvt_pk_f16_f32 v4, v6, v5
	v_pk_mul_f32 v[6:7], v[24:25], v[8:9] op_sel:[0,1]
	s_nop 0
	v_pk_fma_f32 v[22:23], v[24:25], v[0:1], v[6:7] op_sel:[0,1,1] op_sel_hi:[1,1,0] neg_lo:[0,0,1] neg_hi:[0,0,1]
	v_pk_fma_f32 v[6:7], v[24:25], v[0:1], v[6:7] op_sel:[0,1,1] op_sel_hi:[1,1,0]
	s_nop 0
	v_cvt_pk_f16_f32 v5, v22, v7
	v_pk_mul_f32 v[6:7], v[82:83], v[10:11] op_sel_hi:[1,0]
	s_nop 0
	v_pk_fma_f32 v[22:23], v[82:83], v[2:3], v[6:7] op_sel:[0,0,1] op_sel_hi:[1,1,0] neg_lo:[0,0,1] neg_hi:[0,0,1]
	v_pk_fma_f32 v[6:7], v[82:83], v[2:3], v[6:7] op_sel:[0,0,1] op_sel_hi:[1,0,0]
	s_nop 0
	v_cvt_pk_f16_f32 v6, v22, v7
	v_mov_b32_e32 v22, v11
	v_pk_mul_f32 v[24:25], v[84:85], v[22:23] op_sel_hi:[1,0]
	s_nop 0
	v_pk_fma_f32 v[40:41], v[84:85], v[38:39], v[24:25] op_sel:[0,0,1] op_sel_hi:[1,0,0] neg_lo:[0,0,1] neg_hi:[0,0,1]
	v_pk_fma_f32 v[24:25], v[84:85], v[38:39], v[24:25] op_sel:[0,0,1] op_sel_hi:[1,0,0]
	s_nop 0
	v_cvt_pk_f16_f32 v7, v40, v25
	v_lshlrev_b64 v[24:25], 1, v[118:119]
	v_lshl_add_u64 v[40:41], s[10:11], 0, v[24:25]
	v_lshl_add_u64 v[40:41], v[40:41], 0, v[16:17]
	v_lshl_add_u64 v[40:41], v[40:41], 0, v[138:139]
	global_store_dwordx4 v[40:41], v[4:7], off sc1
	s_nop 1
	v_pk_mul_f32 v[4:5], v[30:31], v[8:9] op_sel_hi:[1,0]
	s_nop 0
	v_pk_fma_f32 v[6:7], v[30:31], v[0:1], v[4:5] op_sel:[0,0,1] op_sel_hi:[1,1,0] neg_lo:[0,0,1] neg_hi:[0,0,1]
	v_pk_fma_f32 v[4:5], v[30:31], v[0:1], v[4:5] op_sel:[0,0,1] op_sel_hi:[1,0,0]
	s_nop 0
	v_cvt_pk_f16_f32 v4, v6, v5
	v_pk_mul_f32 v[6:7], v[32:33], v[8:9] op_sel:[0,1]
	s_nop 0
	v_pk_fma_f32 v[8:9], v[32:33], v[0:1], v[6:7] op_sel:[0,1,1] op_sel_hi:[1,1,0] neg_lo:[0,0,1] neg_hi:[0,0,1]
	v_pk_fma_f32 v[0:1], v[32:33], v[0:1], v[6:7] op_sel:[0,1,1] op_sel_hi:[1,1,0]
	s_nop 0
	v_cvt_pk_f16_f32 v5, v8, v1
	v_pk_mul_f32 v[0:1], v[26:27], v[10:11] op_sel_hi:[1,0]
	s_nop 0
	v_pk_fma_f32 v[6:7], v[26:27], v[2:3], v[0:1] op_sel:[0,0,1] op_sel_hi:[1,1,0] neg_lo:[0,0,1] neg_hi:[0,0,1]
	v_pk_fma_f32 v[0:1], v[26:27], v[2:3], v[0:1] op_sel:[0,0,1] op_sel_hi:[1,0,0]
	s_nop 0
	v_cvt_pk_f16_f32 v6, v6, v1
	v_pk_mul_f32 v[0:1], v[28:29], v[22:23] op_sel_hi:[1,0]
	s_nop 0
	v_pk_fma_f32 v[2:3], v[28:29], v[38:39], v[0:1] op_sel:[0,0,1] op_sel_hi:[1,0,0] neg_lo:[0,0,1] neg_hi:[0,0,1]
	v_pk_fma_f32 v[0:1], v[28:29], v[38:39], v[0:1] op_sel:[0,0,1] op_sel_hi:[1,0,0]
	v_cvt_pk_f16_f32 v3, v48, v49
	v_cvt_pk_f16_f32 v7, v2, v1
	v_lshl_add_u64 v[0:1], s[12:13], 0, v[24:25]
	v_lshl_add_u64 v[0:1], v[0:1], 0, v[16:17]
	v_lshl_add_u64 v[0:1], v[0:1], 0, v[138:139]
	global_store_dwordx4 v[0:1], v[4:7], off sc1
	v_lshlrev_b64 v[0:1], 18, v[18:19]
	v_lshlrev_b32_e32 v2, 7, v145
	v_lshl_add_u64 v[0:1], s[14:15], 0, v[0:1]
	v_and_b32_e32 v16, 0x3e000, v2
	v_lshl_add_u64 v[0:1], v[0:1], 0, v[16:17]
	v_lshlrev_b32_e32 v16, 4, v20
	v_lshl_add_u64 v[4:5], v[0:1], 0, v[16:17]
	v_lshlrev_b32_e32 v16, 12, v144
	v_cvt_pk_f16_f32 v2, v46, v47
	v_cvt_pk_f16_f32 v1, v72, v73
	v_cvt_pk_f16_f32 v0, v70, v71
	v_lshl_add_u64 v[4:5], v[4:5], 0, v[16:17]
	global_store_dwordx4 v[4:5], v[0:3], off sc1
	s_nop 1
	v_cvt_pk_f16_f32 v3, v36, v37
	v_cvt_pk_f16_f32 v2, v34, v35
	v_cvt_pk_f16_f32 v1, v60, v61
	v_cvt_pk_f16_f32 v0, v58, v59
	global_store_dwordx4 v[4:5], v[0:3], off offset:1024 sc1
	s_nop 1
	v_cvt_pk_f16_f32 v3, v64, v65
	v_cvt_pk_f16_f32 v2, v62, v63
	v_cvt_pk_f16_f32 v1, v14, v15
	v_cvt_pk_f16_f32 v0, v12, v13
	global_store_dwordx4 v[4:5], v[0:3], off offset:2048 sc1
	s_nop 1
	v_cvt_pk_f16_f32 v3, v52, v53
	v_cvt_pk_f16_f32 v2, v50, v51
	v_cvt_pk_f16_f32 v1, v80, v81
	v_cvt_pk_f16_f32 v0, v78, v79
	global_store_dwordx4 v[4:5], v[0:3], off offset:3072 sc1
	s_endpgm
	.p2align	8

	.amdhsa_kernel _Z9gemm_gldsILi256ELi192ELi4ELi2ELi2ELi4ELi8ELi0ELi4096ELi3072ELi1024EEvPKDF16_S1_PfPKfS4_PKiPDF16_S7_S7_
		.amdhsa_group_segment_fixed_size 114688
		.amdhsa_private_segment_fixed_size 0
		.amdhsa_kernarg_size 72
		.amdhsa_user_sgpr_count 2
		.amdhsa_user_sgpr_dispatch_ptr 0
		.amdhsa_user_sgpr_queue_ptr 0
		.amdhsa_user_sgpr_kernarg_segment_ptr 1
		.amdhsa_user_sgpr_dispatch_id 0
		.amdhsa_user_sgpr_kernarg_preload_length 0
		.amdhsa_user_sgpr_kernarg_preload_offset 0
		.amdhsa_user_sgpr_private_segment_size 0
		.amdhsa_uses_dynamic_stack 0
		.amdhsa_enable_private_segment 0
		.amdhsa_system_sgpr_workgroup_id_x 1
		.amdhsa_system_sgpr_workgroup_id_y 0
		.amdhsa_system_sgpr_workgroup_id_z 0
		.amdhsa_system_sgpr_workgroup_info 0
		.amdhsa_system_vgpr_workitem_id 0
		.amdhsa_next_free_vgpr 253
		.amdhsa_next_free_sgpr 96
		.amdhsa_accum_offset 256
		.amdhsa_reserve_vcc 0
		.amdhsa_float_round_mode_32 0
		.amdhsa_float_round_mode_16_64 0
		.amdhsa_float_denorm_mode_32 3
		.amdhsa_float_denorm_mode_16_64 3
		.amdhsa_dx10_clamp 1
		.amdhsa_ieee_mode 1
		.amdhsa_fp16_overflow 0
		.amdhsa_tg_split 0
		.amdhsa_exception_fp_ieee_invalid_op 0
		.amdhsa_exception_fp_denorm_src 0
		.amdhsa_exception_fp_ieee_div_zero 0
		.amdhsa_exception_fp_ieee_overflow 0
		.amdhsa_exception_fp_ieee_underflow 0
		.amdhsa_exception_fp_ieee_inexact 0
		.amdhsa_exception_int_div_zero 0
	.end_amdhsa_kernel

amdhsa.kernels:
  - .agpr_count:     0
    .args:
      - .actual_access:  read_only
        .address_space:  global
        .offset:         0
        .size:           8
        .value_kind:     global_buffer
      - .actual_access:  read_only
        .address_space:  global
        .offset:         8
        .size:           8
        .value_kind:     global_buffer
      - .actual_access:  read_only
        .address_space:  global
        .offset:         16
        .size:           8
        .value_kind:     global_buffer
      - .actual_access:  read_only
        .address_space:  global
        .offset:         24
        .size:           8
        .value_kind:     global_buffer
      - .actual_access:  read_only
        .address_space:  global
        .offset:         32
        .size:           8
        .value_kind:     global_buffer
      - .actual_access:  read_only
        .address_space:  global
        .offset:         40
        .size:           8
        .value_kind:     global_buffer
      - .actual_access:  write_only
        .address_space:  global
        .offset:         48
        .size:           8
        .value_kind:     global_buffer
      - .actual_access:  write_only
        .address_space:  global
        .offset:         56
        .size:           8
        .value_kind:     global_buffer
      - .actual_access:  write_only
        .address_space:  global
        .offset:         64
        .size:           8
        .value_kind:     global_buffer
      - .actual_access:  write_only
        .address_space:  global
        .offset:         72
        .size:           8
        .value_kind:     global_buffer
      - .actual_access:  write_only
        .address_space:  global
        .offset:         80
        .size:           8
        .value_kind:     global_buffer
    .group_segment_fixed_size: 16640
    .kernarg_segment_align: 8
    .kernarg_segment_size: 88
    .language:       OpenCL C
    .language_version:
      - 2
      - 0
    .max_flat_workgroup_size: 256
    .name:           _Z11prep_kernelPKfS0_S0_S0_S0_PKiPDF16_S3_S3_PyPi
    .private_segment_fixed_size: 0
    .sgpr_count:     54
    .sgpr_spill_count: 0
    .symbol:         _Z11prep_kernelPKfS0_S0_S0_S0_PKiPDF16_S3_S3_PyPi.kd
    .uniform_work_group_size: 1
    .uses_dynamic_stack: false
    .vgpr_count:     46
    .vgpr_spill_count: 0
    .wavefront_size: 64
  - .agpr_count:     0
    .args:
      - .actual_access:  read_only
        .address_space:  global
        .offset:         0
        .size:           8
        .value_kind:     global_buffer
      - .actual_access:  read_only
        .address_space:  global
        .offset:         8
        .size:           8
        .value_kind:     global_buffer
      - .actual_access:  read_only
        .address_space:  global
        .offset:         16
        .size:           8
        .value_kind:     global_buffer
      - .actual_access:  read_only
        .address_space:  global
        .offset:         24
        .size:           8
        .value_kind:     global_buffer
      - .actual_access:  read_only
        .address_space:  global
        .offset:         32
        .size:           8
        .value_kind:     global_buffer
      - .actual_access:  write_only
        .address_space:  global
        .offset:         40
        .size:           8
        .value_kind:     global_buffer
    .group_segment_fixed_size: 36864
    .kernarg_segment_align: 8
    .kernarg_segment_size: 48
    .language:       OpenCL C
    .language_version:
      - 2
      - 0
    .max_flat_workgroup_size: 256
    .name:           _Z11attn_kernelPKDF16_S0_S0_PKyPKiPDF16_
    .private_segment_fixed_size: 0
    .sgpr_count:     32
    .sgpr_spill_count: 0
    .symbol:         _Z11attn_kernelPKDF16_S0_S0_PKyPKiPDF16_.kd
    .uniform_work_group_size: 1
    .uses_dynamic_stack: false
    .vgpr_count:     114
    .vgpr_spill_count: 0
    .wavefront_size: 64
  - .agpr_count:     0
    .args:
      - .address_space:  global
        .offset:         0
        .size:           8
        .value_kind:     global_buffer
      - .address_space:  global
        .offset:         8
        .size:           8
        .value_kind:     global_buffer
      - .actual_access:  read_only
        .address_space:  global
        .offset:         16
        .size:           8
        .value_kind:     global_buffer
      - .actual_access:  read_only
        .address_space:  global
        .offset:         24
        .size:           8
        .value_kind:     global_buffer
      - .actual_access:  read_only
        .address_space:  global
        .offset:         32
        .size:           8
        .value_kind:     global_buffer
      - .actual_access:  read_only
        .address_space:  global
        .offset:         40
        .size:           8
        .value_kind:     global_buffer
      - .actual_access:  write_only
        .address_space:  global
        .offset:         48
        .size:           8
        .value_kind:     global_buffer
      - .actual_access:  write_only
        .address_space:  global
        .offset:         56
        .size:           8
        .value_kind:     global_buffer
      - .actual_access:  write_only
        .address_space:  global
        .offset:         64
        .size:           8
        .value_kind:     global_buffer
    .group_segment_fixed_size: 114688
    .kernarg_segment_align: 8
    .kernarg_segment_size: 72
    .language:       OpenCL C
    .language_version:
      - 2
      - 0
    .max_flat_workgroup_size: 512
    .name:           _Z9gemm_gldsILi256ELi192ELi4ELi2ELi2ELi4ELi8ELi0ELi4096ELi3072ELi1024EEvPKDF16_S1_PfPKfS4_PKiPDF16_S7_S7_
    .private_segment_fixed_size: 0
    .sgpr_count:     29
    .sgpr_spill_count: 0
    .symbol:         _Z9gemm_gldsILi256ELi192ELi4ELi2ELi2ELi4ELi8ELi0ELi4096ELi3072ELi1024EEvPKDF16_S1_PfPKfS4_PKiPDF16_S7_S7_.kd
    .uniform_work_group_size: 1
    .uses_dynamic_stack: false
    .vgpr_count:     253
    .vgpr_spill_count: 0
    .wavefront_size: 64
  - .agpr_count:     0
    .args:
      - .address_space:  global
        .offset:         0
        .size:           8
        .value_kind:     global_buffer
      - .address_space:  global
        .offset:         8
        .size:           8
        .value_kind:     global_buffer
      - .actual_access:  write_only
        .address_space:  global
        .offset:         16
        .size:           8
        .value_kind:     global_buffer
      - .actual_access:  read_only
        .address_space:  global
        .offset:         24
        .size:           8
        .value_kind:     global_buffer
      - .actual_access:  read_only
        .address_space:  global
        .offset:         32
        .size:           8
        .value_kind:     global_buffer
      - .actual_access:  read_only
        .address_space:  global
        .offset:         40
        .size:           8
        .value_kind:     global_buffer
      - .actual_access:  read_only
        .address_space:  global
        .offset:         48
        .size:           8
        .value_kind:     global_buffer
      - .actual_access:  read_only
        .address_space:  global
        .offset:         56
        .size:           8
        .value_kind:     global_buffer
      - .actual_access:  read_only
        .address_space:  global
        .offset:         64
        .size:           8
        .value_kind:     global_buffer
    .group_segment_fixed_size: 98304
    .kernarg_segment_align: 8
    .kernarg_segment_size: 72
    .language:       OpenCL C
    .language_version:
      - 2
      - 0
    .max_flat_workgroup_size: 512
    .name:           _Z9gemm_gldsILi128ELi128ELi4ELi2ELi3ELi8ELi4ELi1ELi4096ELi1024ELi1024EEvPKDF16_S1_PfPKfS4_PKiPDF16_S7_S7_
    .private_segment_fixed_size: 0
    .sgpr_count:     20
    .sgpr_spill_count: 0
    .symbol:         _Z9gemm_gldsILi128ELi128ELi4ELi2ELi3ELi8ELi4ELi1ELi4096ELi1024ELi1024EEvPKDF16_S1_PfPKfS4_PKiPDF16_S7_S7_.kd
    .uniform_work_group_size: 1
    .uses_dynamic_stack: false
    .vgpr_count:     92
    .vgpr_spill_count: 0
    .wavefront_size: 64
